# S1 + realign barrier of waves 0-3 moved behind their int-to-float conversions in the in-projection and SwiGLU epilogues
# baseline (speedup 1.0000x reference)
.LBB0_478:
	s_cmp_gt_u32 s92, 13
	s_cselect_b64 s[80:81], -1, 0
	s_and_b64 vcc, s[80:81], exec
	s_cselect_b32 s0, -14, 2
	s_add_i32 s80, s0, s92
	s_ashr_i32 s81, s80, 31
	s_lshl_b64 s[80:81], s[80:81], 7
	s_add_u32 s0, s76, s80
	s_addc_u32 s1, s77, s81
	s_add_u32 s82, s42, s80
	s_addc_u32 s83, s43, s81
	s_cmp_gt_u32 s92, 12
	s_cselect_b32 s80, -13, 3
	s_add_i32 s80, s80, s92
	s_ashr_i32 s81, s80, 31
	s_lshl_b64 s[80:81], s[80:81], 7
	s_add_u32 s94, s76, s80
	s_addc_u32 s50, s77, s81
	s_add_u32 s16, s42, s80
	s_addc_u32 s17, s43, s81
	s_cmp_eq_u32 s92, 14
	s_cselect_b32 s84, s70, s0
	s_mov_b32 s0, s92
	v_add_u32_e32 v140, 0x10000, v173
	v_add_u32_e32 v156, 0x14000, v173
	ds_read_b128 v[128:131], v140
	ds_read_b128 v[132:135], v140 offset:1024
	ds_read_b128 v[136:139], v140 offset:2048
	ds_read_b128 v[140:143], v140 offset:3072
	ds_read_b128 v[144:147], v156
	ds_read_b128 v[148:151], v156 offset:1024
	ds_read_b128 v[152:155], v156 offset:2048
	ds_read_b128 v[166:169], v156 offset:3072
	s_cselect_b32 s85, s63, s1
	s_cselect_b32 s87, s72, s83
	s_cselect_b32 s86, s75, s82
	s_cselect_b32 s81, s10, s50
	s_cselect_b32 s80, s9, s94
	s_cselect_b32 s83, s12, s17
	s_cselect_b32 s82, s11, s16
	ds_read_b128 v[176:179], v174
	ds_read_b128 v[180:183], v174 offset:1024
	ds_read_b128 v[184:187], v174 offset:2048
	ds_read_b128 v[190:193], v174 offset:3072
	ds_read_b128 v[194:197], v174 offset:4096
	ds_read_b128 v[198:201], v174 offset:5120
	ds_read_b128 v[202:205], v174 offset:6144
	ds_read_b128 v[206:209], v174 offset:7168
	s_add_u32 s0, s78, 0x40080
	s_addc_u32 s1, s79, 0
	s_mov_b32 m0, s89
	s_nop 0
	global_load_lds_dwordx4 v165, s[0:1]
	s_add_i32 s16, s19, 0xe000
	s_mov_b32 m0, s16
	s_nop 0
	global_load_lds_dwordx4 v171, s[0:1]
	s_setprio 1
	s_waitcnt vmcnt(8)
	s_waitcnt lgkmcnt(0)
	s_barrier
	v_mfma_i32_16x16x64_i8 v[124:127], v[128:131], v[176:179], v[124:127]
	v_mfma_i32_16x16x64_i8 v[120:123], v[136:139], v[176:179], v[120:123]
	v_mfma_i32_16x16x64_i8 v[116:119], v[128:131], v[184:187], v[116:119]
	v_mfma_i32_16x16x64_i8 v[108:111], v[136:139], v[184:187], v[108:111]
	v_mfma_i32_16x16x64_i8 v[100:103], v[128:131], v[194:197], v[100:103]
	v_mfma_i32_16x16x64_i8 v[92:95], v[136:139], v[194:197], v[92:95]
	v_mfma_i32_16x16x64_i8 v[84:87], v[128:131], v[202:205], v[84:87]
	v_mfma_i32_16x16x64_i8 v[76:79], v[136:139], v[202:205], v[76:79]
	v_mfma_i32_16x16x64_i8 v[124:127], v[132:135], v[180:183], v[124:127]
	v_mfma_i32_16x16x64_i8 v[120:123], v[140:143], v[180:183], v[120:123]
	v_mfma_i32_16x16x64_i8 v[116:119], v[132:135], v[190:193], v[116:119]
	v_mfma_i32_16x16x64_i8 v[108:111], v[140:143], v[190:193], v[108:111]
	v_mfma_i32_16x16x64_i8 v[100:103], v[132:135], v[198:201], v[100:103]
	v_mfma_i32_16x16x64_i8 v[92:95], v[140:143], v[198:201], v[92:95]
	v_mfma_i32_16x16x64_i8 v[84:87], v[132:135], v[206:209], v[84:87]
	v_mfma_i32_16x16x64_i8 v[76:79], v[140:143], v[206:209], v[76:79]
	v_mfma_i32_16x16x64_i8 v[112:115], v[144:147], v[176:179], v[112:115]
	v_mfma_i32_16x16x64_i8 v[104:107], v[152:155], v[176:179], v[104:107]
	v_mfma_i32_16x16x64_i8 v[96:99], v[144:147], v[184:187], v[96:99]
	v_mfma_i32_16x16x64_i8 v[88:91], v[152:155], v[184:187], v[88:91]
	v_mfma_i32_16x16x64_i8 v[80:83], v[144:147], v[194:197], v[80:83]
	v_mfma_i32_16x16x64_i8 v[72:75], v[152:155], v[194:197], v[72:75]
	v_mfma_i32_16x16x64_i8 v[68:71], v[144:147], v[202:205], v[68:71]
	v_mfma_i32_16x16x64_i8 v[64:67], v[152:155], v[202:205], v[64:67]
	v_mfma_i32_16x16x64_i8 v[112:115], v[148:151], v[180:183], v[112:115]
	v_mfma_i32_16x16x64_i8 v[104:107], v[166:169], v[180:183], v[104:107]
	v_mfma_i32_16x16x64_i8 v[96:99], v[148:151], v[190:193], v[96:99]
	v_mfma_i32_16x16x64_i8 v[88:91], v[166:169], v[190:193], v[88:91]
	v_mfma_i32_16x16x64_i8 v[80:83], v[148:151], v[198:201], v[80:83]
	v_mfma_i32_16x16x64_i8 v[72:75], v[166:169], v[198:201], v[72:75]
	v_mfma_i32_16x16x64_i8 v[68:71], v[148:151], v[206:209], v[68:71]
	v_mfma_i32_16x16x64_i8 v[64:67], v[166:169], v[206:209], v[64:67]
	s_barrier
	s_setprio 0
	ds_read_b128 v[176:179], v174 offset:16384
	ds_read_b128 v[180:183], v174 offset:17408
	ds_read_b128 v[184:187], v174 offset:18432
	ds_read_b128 v[190:193], v174 offset:19456
	ds_read_b128 v[194:197], v174 offset:20480
	ds_read_b128 v[198:201], v174 offset:21504
	ds_read_b128 v[202:205], v174 offset:22528
	ds_read_b128 v[206:209], v174 offset:23552
	s_mov_b32 m0, s27
	s_nop 0
	global_load_lds_dwordx4 v170, s[86:87]
	s_nop 0
	s_mov_b32 m0, s28
	s_nop 0
	global_load_lds_dwordx4 v172, s[86:87]
	s_add_u32 s0, s86, 0x40000
	s_addc_u32 s1, s87, 0
	s_mov_b32 m0, s29
	s_nop 0
	global_load_lds_dwordx4 v170, s[0:1]
	s_nop 0
	s_mov_b32 m0, s34
	s_nop 0
	global_load_lds_dwordx4 v172, s[0:1]
	s_mov_b32 m0, s19
	s_nop 0
	global_load_lds_dwordx4 v165, s[84:85]
	s_nop 0
	s_mov_b32 m0, s35
	s_nop 0
	global_load_lds_dwordx4 v171, s[84:85]
	s_setprio 1
	s_waitcnt vmcnt(8)
	s_waitcnt lgkmcnt(0)
	s_barrier
	v_mfma_i32_16x16x64_i8 v[60:63], v[128:131], v[176:179], v[60:63]
	v_mfma_i32_16x16x64_i8 v[56:59], v[136:139], v[176:179], v[56:59]
	v_mfma_i32_16x16x64_i8 v[52:55], v[128:131], v[184:187], v[52:55]
	v_mfma_i32_16x16x64_i8 v[44:47], v[136:139], v[184:187], v[44:47]
	v_mfma_i32_16x16x64_i8 v[36:39], v[128:131], v[194:197], v[36:39]
	v_mfma_i32_16x16x64_i8 v[28:31], v[136:139], v[194:197], v[28:31]
	v_mfma_i32_16x16x64_i8 v[20:23], v[128:131], v[202:205], v[20:23]
	v_mfma_i32_16x16x64_i8 v[12:15], v[136:139], v[202:205], v[12:15]
	v_mfma_i32_16x16x64_i8 v[60:63], v[132:135], v[180:183], v[60:63]
	v_mfma_i32_16x16x64_i8 v[56:59], v[140:143], v[180:183], v[56:59]
	v_mfma_i32_16x16x64_i8 v[52:55], v[132:135], v[190:193], v[52:55]
	v_mfma_i32_16x16x64_i8 v[44:47], v[140:143], v[190:193], v[44:47]
	v_mfma_i32_16x16x64_i8 v[36:39], v[132:135], v[198:201], v[36:39]
	v_mfma_i32_16x16x64_i8 v[28:31], v[140:143], v[198:201], v[28:31]
	v_mfma_i32_16x16x64_i8 v[20:23], v[132:135], v[206:209], v[20:23]
	v_mfma_i32_16x16x64_i8 v[12:15], v[140:143], v[206:209], v[12:15]
	v_mfma_i32_16x16x64_i8 v[48:51], v[144:147], v[176:179], v[48:51]
	v_mfma_i32_16x16x64_i8 v[40:43], v[152:155], v[176:179], v[40:43]
	v_mfma_i32_16x16x64_i8 v[32:35], v[144:147], v[184:187], v[32:35]
	v_mfma_i32_16x16x64_i8 v[24:27], v[152:155], v[184:187], v[24:27]
	v_mfma_i32_16x16x64_i8 v[16:19], v[144:147], v[194:197], v[16:19]
	v_mfma_i32_16x16x64_i8 v[8:11], v[152:155], v[194:197], v[8:11]
	v_mfma_i32_16x16x64_i8 v[4:7], v[144:147], v[202:205], v[4:7]
	v_mfma_i32_16x16x64_i8 v[0:3], v[152:155], v[202:205], v[0:3]
	v_mfma_i32_16x16x64_i8 v[48:51], v[148:151], v[180:183], v[48:51]
	v_mfma_i32_16x16x64_i8 v[40:43], v[166:169], v[180:183], v[40:43]
	v_mfma_i32_16x16x64_i8 v[32:35], v[148:151], v[190:193], v[32:35]
	v_mfma_i32_16x16x64_i8 v[24:27], v[166:169], v[190:193], v[24:27]
	v_mfma_i32_16x16x64_i8 v[16:19], v[148:151], v[198:201], v[16:19]
	v_mfma_i32_16x16x64_i8 v[8:11], v[166:169], v[198:201], v[8:11]
	v_mfma_i32_16x16x64_i8 v[4:7], v[148:151], v[206:209], v[4:7]
	v_mfma_i32_16x16x64_i8 v[0:3], v[166:169], v[206:209], v[0:3]
	s_barrier
	s_setprio 0
	v_add_u32_e32 v140, 0x18000, v173
	v_add_u32_e32 v156, 0x1c000, v173
	ds_read_b128 v[128:131], v140
	ds_read_b128 v[132:135], v140 offset:1024
	ds_read_b128 v[136:139], v140 offset:2048
	ds_read_b128 v[140:143], v140 offset:3072
	ds_read_b128 v[144:147], v156
	ds_read_b128 v[148:151], v156 offset:1024
	ds_read_b128 v[152:155], v156 offset:2048
	ds_read_b128 v[166:169], v156 offset:3072
	ds_read_b128 v[176:179], v174 offset:32768
	ds_read_b128 v[180:183], v174 offset:33792
	ds_read_b128 v[184:187], v174 offset:34816
	ds_read_b128 v[190:193], v174 offset:35840
	ds_read_b128 v[194:197], v174 offset:36864
	ds_read_b128 v[198:201], v174 offset:37888
	ds_read_b128 v[202:205], v174 offset:38912
	ds_read_b128 v[206:209], v174 offset:39936
	s_add_u32 s0, s84, 0x40000
	s_addc_u32 s1, s85, 0
	s_mov_b32 m0, s36
	s_nop 0
	global_load_lds_dwordx4 v165, s[0:1]
	s_nop 0
	s_mov_b32 m0, s37
	s_nop 0
	global_load_lds_dwordx4 v171, s[0:1]
	s_setprio 1
	s_waitcnt vmcnt(8)
	s_waitcnt lgkmcnt(0)
	s_barrier
	v_mfma_i32_16x16x64_i8 v[124:127], v[128:131], v[176:179], v[124:127]
	v_mfma_i32_16x16x64_i8 v[120:123], v[136:139], v[176:179], v[120:123]
	v_mfma_i32_16x16x64_i8 v[116:119], v[128:131], v[184:187], v[116:119]
	v_mfma_i32_16x16x64_i8 v[108:111], v[136:139], v[184:187], v[108:111]
	v_mfma_i32_16x16x64_i8 v[100:103], v[128:131], v[194:197], v[100:103]
	v_mfma_i32_16x16x64_i8 v[92:95], v[136:139], v[194:197], v[92:95]
	v_mfma_i32_16x16x64_i8 v[84:87], v[128:131], v[202:205], v[84:87]
	v_mfma_i32_16x16x64_i8 v[76:79], v[136:139], v[202:205], v[76:79]
	v_mfma_i32_16x16x64_i8 v[124:127], v[132:135], v[180:183], v[124:127]
	v_mfma_i32_16x16x64_i8 v[120:123], v[140:143], v[180:183], v[120:123]
	v_mfma_i32_16x16x64_i8 v[116:119], v[132:135], v[190:193], v[116:119]
	v_mfma_i32_16x16x64_i8 v[108:111], v[140:143], v[190:193], v[108:111]
	v_mfma_i32_16x16x64_i8 v[100:103], v[132:135], v[198:201], v[100:103]
	v_mfma_i32_16x16x64_i8 v[92:95], v[140:143], v[198:201], v[92:95]
	v_mfma_i32_16x16x64_i8 v[84:87], v[132:135], v[206:209], v[84:87]
	v_mfma_i32_16x16x64_i8 v[76:79], v[140:143], v[206:209], v[76:79]
	v_mfma_i32_16x16x64_i8 v[112:115], v[144:147], v[176:179], v[112:115]
	v_mfma_i32_16x16x64_i8 v[104:107], v[152:155], v[176:179], v[104:107]
	v_mfma_i32_16x16x64_i8 v[96:99], v[144:147], v[184:187], v[96:99]
	v_mfma_i32_16x16x64_i8 v[88:91], v[152:155], v[184:187], v[88:91]
	v_mfma_i32_16x16x64_i8 v[80:83], v[144:147], v[194:197], v[80:83]
	v_mfma_i32_16x16x64_i8 v[72:75], v[152:155], v[194:197], v[72:75]
	v_mfma_i32_16x16x64_i8 v[68:71], v[144:147], v[202:205], v[68:71]
	v_mfma_i32_16x16x64_i8 v[64:67], v[152:155], v[202:205], v[64:67]
	v_mfma_i32_16x16x64_i8 v[112:115], v[148:151], v[180:183], v[112:115]
	v_mfma_i32_16x16x64_i8 v[104:107], v[166:169], v[180:183], v[104:107]
	v_mfma_i32_16x16x64_i8 v[96:99], v[148:151], v[190:193], v[96:99]
	v_mfma_i32_16x16x64_i8 v[88:91], v[166:169], v[190:193], v[88:91]
	v_mfma_i32_16x16x64_i8 v[80:83], v[148:151], v[198:201], v[80:83]
	v_mfma_i32_16x16x64_i8 v[72:75], v[166:169], v[198:201], v[72:75]
	v_mfma_i32_16x16x64_i8 v[68:71], v[148:151], v[206:209], v[68:71]
	v_mfma_i32_16x16x64_i8 v[64:67], v[166:169], v[206:209], v[64:67]
	s_barrier
	s_setprio 0
	ds_read_b128 v[176:179], v174 offset:49152
	ds_read_b128 v[180:183], v174 offset:50176
	ds_read_b128 v[184:187], v174 offset:51200
	ds_read_b128 v[190:193], v174 offset:52224
	ds_read_b128 v[194:197], v174 offset:53248
	ds_read_b128 v[198:201], v174 offset:54272
	ds_read_b128 v[202:205], v174 offset:55296
	ds_read_b128 v[206:209], v174 offset:56320
	s_mov_b32 m0, s66
	s_nop 0
	global_load_lds_dwordx4 v170, s[82:83]
	s_nop 0
	s_mov_b32 m0, s67
	s_nop 0
	global_load_lds_dwordx4 v172, s[82:83]
	s_add_u32 s0, s82, 0x40000
	s_addc_u32 s1, s83, 0
	s_mov_b32 m0, s71
	s_nop 0
	global_load_lds_dwordx4 v170, s[0:1]
	s_nop 0
	s_mov_b32 m0, s88
	s_nop 0
	global_load_lds_dwordx4 v172, s[0:1]
	s_mov_b32 m0, s68
	s_nop 0
	global_load_lds_dwordx4 v165, s[80:81]
	s_nop 0
	s_mov_b32 m0, s69
	s_nop 0
	global_load_lds_dwordx4 v171, s[80:81]
	s_setprio 1
	s_waitcnt vmcnt(8)
	s_waitcnt lgkmcnt(0)
	s_barrier
	v_mfma_i32_16x16x64_i8 v[60:63], v[128:131], v[176:179], v[60:63]
	v_mfma_i32_16x16x64_i8 v[56:59], v[136:139], v[176:179], v[56:59]
	v_mfma_i32_16x16x64_i8 v[52:55], v[128:131], v[184:187], v[52:55]
	v_mfma_i32_16x16x64_i8 v[44:47], v[136:139], v[184:187], v[44:47]
	v_mfma_i32_16x16x64_i8 v[36:39], v[128:131], v[194:197], v[36:39]
	v_mfma_i32_16x16x64_i8 v[28:31], v[136:139], v[194:197], v[28:31]
	v_mfma_i32_16x16x64_i8 v[20:23], v[128:131], v[202:205], v[20:23]
	v_mfma_i32_16x16x64_i8 v[12:15], v[136:139], v[202:205], v[12:15]
	v_mfma_i32_16x16x64_i8 v[60:63], v[132:135], v[180:183], v[60:63]
	v_mfma_i32_16x16x64_i8 v[56:59], v[140:143], v[180:183], v[56:59]
	v_mfma_i32_16x16x64_i8 v[52:55], v[132:135], v[190:193], v[52:55]
	v_mfma_i32_16x16x64_i8 v[44:47], v[140:143], v[190:193], v[44:47]
	v_mfma_i32_16x16x64_i8 v[36:39], v[132:135], v[198:201], v[36:39]
	v_mfma_i32_16x16x64_i8 v[28:31], v[140:143], v[198:201], v[28:31]
	v_mfma_i32_16x16x64_i8 v[20:23], v[132:135], v[206:209], v[20:23]
	v_mfma_i32_16x16x64_i8 v[12:15], v[140:143], v[206:209], v[12:15]
	v_mfma_i32_16x16x64_i8 v[48:51], v[144:147], v[176:179], v[48:51]
	v_mfma_i32_16x16x64_i8 v[40:43], v[152:155], v[176:179], v[40:43]
	v_mfma_i32_16x16x64_i8 v[32:35], v[144:147], v[184:187], v[32:35]
	v_mfma_i32_16x16x64_i8 v[24:27], v[152:155], v[184:187], v[24:27]
	v_mfma_i32_16x16x64_i8 v[16:19], v[144:147], v[194:197], v[16:19]
	v_mfma_i32_16x16x64_i8 v[8:11], v[152:155], v[194:197], v[8:11]
	v_mfma_i32_16x16x64_i8 v[4:7], v[144:147], v[202:205], v[4:7]
	v_mfma_i32_16x16x64_i8 v[0:3], v[152:155], v[202:205], v[0:3]
	v_mfma_i32_16x16x64_i8 v[48:51], v[148:151], v[180:183], v[48:51]
	v_mfma_i32_16x16x64_i8 v[40:43], v[166:169], v[180:183], v[40:43]
	v_mfma_i32_16x16x64_i8 v[32:35], v[148:151], v[190:193], v[32:35]
	v_mfma_i32_16x16x64_i8 v[24:27], v[166:169], v[190:193], v[24:27]
	v_mfma_i32_16x16x64_i8 v[16:19], v[148:151], v[198:201], v[16:19]
	v_mfma_i32_16x16x64_i8 v[8:11], v[166:169], v[198:201], v[8:11]
	v_mfma_i32_16x16x64_i8 v[4:7], v[148:151], v[206:209], v[4:7]
	v_mfma_i32_16x16x64_i8 v[0:3], v[166:169], v[206:209], v[0:3]
	s_barrier
	s_setprio 0
	s_add_i32 s92, s92, 2
	s_add_u32 s78, s78, 0x100
	s_addc_u32 s79, s79, 0
	s_cbranch_vccz .LBB0_478
	v_cvt_f32_i32_e32 v124, v124
	v_cvt_f32_i32_e32 v125, v125
	v_cvt_f32_i32_e32 v162, v126
	v_cvt_f32_i32_e32 v163, v127
	v_cvt_f32_i32_e32 v120, v120
	v_cvt_f32_i32_e32 v121, v121
	v_cvt_f32_i32_e32 v122, v122
	v_cvt_f32_i32_e32 v123, v123
	v_cvt_f32_i32_e32 v116, v116
	v_cvt_f32_i32_e32 v117, v117
	v_cvt_f32_i32_e32 v118, v118
	v_cvt_f32_i32_e32 v119, v119
	v_cvt_f32_i32_e32 v108, v108
	v_cvt_f32_i32_e32 v109, v109
	v_cvt_f32_i32_e32 v110, v110
	v_cvt_f32_i32_e32 v111, v111
	v_cvt_f32_i32_e32 v100, v100
	v_cvt_f32_i32_e32 v101, v101
	v_cvt_f32_i32_e32 v102, v102
	v_cvt_f32_i32_e32 v103, v103
	v_cvt_f32_i32_e32 v92, v92
	v_cvt_f32_i32_e32 v93, v93
	v_cvt_f32_i32_e32 v94, v94
	v_cvt_f32_i32_e32 v95, v95
	v_cvt_f32_i32_e32 v84, v84
	v_cvt_f32_i32_e32 v85, v85
	v_cvt_f32_i32_e32 v86, v86
	v_cvt_f32_i32_e32 v87, v87
	v_cvt_f32_i32_e32 v76, v76
	v_cvt_f32_i32_e32 v77, v77
	v_cvt_f32_i32_e32 v78, v78
	v_cvt_f32_i32_e32 v79, v79
	v_cvt_f32_i32_e32 v112, v112
	v_cvt_f32_i32_e32 v113, v113
	v_cvt_f32_i32_e32 v114, v114
	v_cvt_f32_i32_e32 v115, v115
	v_cvt_f32_i32_e32 v104, v104
	v_cvt_f32_i32_e32 v105, v105
	v_cvt_f32_i32_e32 v106, v106
	v_cvt_f32_i32_e32 v107, v107
	v_cvt_f32_i32_e32 v96, v96
	v_cvt_f32_i32_e32 v97, v97
	v_cvt_f32_i32_e32 v98, v98
	v_cvt_f32_i32_e32 v99, v99
	v_cvt_f32_i32_e32 v88, v88
	v_cvt_f32_i32_e32 v89, v89
	v_cvt_f32_i32_e32 v90, v90
	v_cvt_f32_i32_e32 v91, v91
	v_cvt_f32_i32_e32 v80, v80
	v_cvt_f32_i32_e32 v81, v81
	v_cvt_f32_i32_e32 v82, v82
	v_cvt_f32_i32_e32 v83, v83
	v_cvt_f32_i32_e32 v72, v72
	v_cvt_f32_i32_e32 v73, v73
	v_cvt_f32_i32_e32 v74, v74
	v_cvt_f32_i32_e32 v75, v75
	v_cvt_f32_i32_e32 v68, v68
	v_cvt_f32_i32_e32 v69, v69
	v_cvt_f32_i32_e32 v70, v70
	v_cvt_f32_i32_e32 v71, v71
	v_cvt_f32_i32_e32 v64, v64
	v_cvt_f32_i32_e32 v65, v65
	v_cvt_f32_i32_e32 v66, v66
	v_cvt_f32_i32_e32 v67, v67
	v_cvt_f32_i32_e32 v60, v60
	v_cvt_f32_i32_e32 v61, v61
	v_cvt_f32_i32_e32 v62, v62
	v_cvt_f32_i32_e32 v63, v63
	v_cvt_f32_i32_e32 v56, v56
	v_cvt_f32_i32_e32 v57, v57
	v_cvt_f32_i32_e32 v58, v58
	v_cvt_f32_i32_e32 v59, v59
	v_cvt_f32_i32_e32 v52, v52
	v_cvt_f32_i32_e32 v53, v53
	v_cvt_f32_i32_e32 v54, v54
	v_cvt_f32_i32_e32 v55, v55
	v_cvt_f32_i32_e32 v44, v44
	v_cvt_f32_i32_e32 v45, v45
	v_cvt_f32_i32_e32 v46, v46
	v_cvt_f32_i32_e32 v47, v47
	v_cvt_f32_i32_e32 v36, v36
	v_cvt_f32_i32_e32 v37, v37
	v_cvt_f32_i32_e32 v38, v38
	v_cvt_f32_i32_e32 v39, v39
	v_cvt_f32_i32_e32 v28, v28
	v_cvt_f32_i32_e32 v29, v29
	v_cvt_f32_i32_e32 v30, v30
	v_cvt_f32_i32_e32 v31, v31
	v_cvt_f32_i32_e32 v20, v20
	v_cvt_f32_i32_e32 v21, v21
	v_cvt_f32_i32_e32 v22, v22
	v_cvt_f32_i32_e32 v23, v23
	v_cvt_f32_i32_e32 v12, v12
	v_cvt_f32_i32_e32 v13, v13
	v_cvt_f32_i32_e32 v14, v14
	v_cvt_f32_i32_e32 v15, v15
	v_cvt_f32_i32_e32 v48, v48
	v_cvt_f32_i32_e32 v49, v49
	v_cvt_f32_i32_e32 v50, v50
	v_cvt_f32_i32_e32 v51, v51
	v_cvt_f32_i32_e32 v40, v40
	v_cvt_f32_i32_e32 v41, v41
	v_cvt_f32_i32_e32 v42, v42
	v_cvt_f32_i32_e32 v43, v43
	v_cvt_f32_i32_e32 v32, v32
	v_cvt_f32_i32_e32 v33, v33
	v_cvt_f32_i32_e32 v34, v34
	v_cvt_f32_i32_e32 v35, v35
	v_cvt_f32_i32_e32 v24, v24
	v_cvt_f32_i32_e32 v25, v25
	v_cvt_f32_i32_e32 v26, v26
	v_cvt_f32_i32_e32 v27, v27
	v_cvt_f32_i32_e32 v16, v16
	v_cvt_f32_i32_e32 v17, v17
	v_cvt_f32_i32_e32 v18, v18
	v_cvt_f32_i32_e32 v19, v19
	v_cvt_f32_i32_e32 v8, v8
	v_cvt_f32_i32_e32 v9, v9
	v_cvt_f32_i32_e32 v10, v10
	v_cvt_f32_i32_e32 v11, v11
	v_cvt_f32_i32_e32 v4, v4
	v_cvt_f32_i32_e32 v5, v5
	v_cvt_f32_i32_e32 v6, v6
	v_cvt_f32_i32_e32 v7, v7
	v_cvt_f32_i32_e32 v0, v0
	v_cvt_f32_i32_e32 v1, v1
	v_cvt_f32_i32_e32 v2, v2
	v_cvt_f32_i32_e32 v3, v3
	s_andn2_b64 vcc, exec, s[40:41]
	s_mov_b32 s70, 0x42b17218
	s_cbranch_vccnz .LBB0_483
	v_mov_b32_e32 v159, v158
	v_pk_mul_f32 v[162:163], v[158:159], v[162:163]
	v_pk_mul_f32 v[124:125], v[160:161], v[124:125]
	v_pk_mul_f32 v[122:123], v[158:159], v[122:123]
	v_pk_mul_f32 v[120:121], v[160:161], v[120:121]
	v_pk_mul_f32 v[118:119], v[158:159], v[118:119]
	v_pk_mul_f32 v[116:117], v[160:161], v[116:117]
	v_pk_mul_f32 v[110:111], v[158:159], v[110:111]
	v_pk_mul_f32 v[108:109], v[160:161], v[108:109]
	v_pk_mul_f32 v[102:103], v[158:159], v[102:103]
	v_pk_mul_f32 v[100:101], v[160:161], v[100:101]
	v_pk_mul_f32 v[94:95], v[158:159], v[94:95]
	v_pk_mul_f32 v[92:93], v[160:161], v[92:93]
	v_pk_mul_f32 v[86:87], v[158:159], v[86:87]
	v_pk_mul_f32 v[84:85], v[160:161], v[84:85]
	v_pk_mul_f32 v[78:79], v[158:159], v[78:79]
	v_pk_mul_f32 v[76:77], v[160:161], v[76:77]
	v_pk_mul_f32 v[114:115], v[158:159], v[114:115]
	v_pk_mul_f32 v[112:113], v[160:161], v[112:113]
	v_pk_mul_f32 v[106:107], v[158:159], v[106:107]
	v_pk_mul_f32 v[104:105], v[160:161], v[104:105]
	v_pk_mul_f32 v[98:99], v[158:159], v[98:99]
	v_pk_mul_f32 v[96:97], v[160:161], v[96:97]
	v_pk_mul_f32 v[90:91], v[158:159], v[90:91]
	v_pk_mul_f32 v[88:89], v[160:161], v[88:89]
	v_pk_mul_f32 v[82:83], v[158:159], v[82:83]
	v_pk_mul_f32 v[80:81], v[160:161], v[80:81]
	v_pk_mul_f32 v[74:75], v[158:159], v[74:75]
	v_pk_mul_f32 v[72:73], v[160:161], v[72:73]
	v_pk_mul_f32 v[70:71], v[158:159], v[70:71]
	v_pk_mul_f32 v[68:69], v[160:161], v[68:69]
	v_pk_mul_f32 v[66:67], v[158:159], v[66:67]
	v_pk_mul_f32 v[64:65], v[160:161], v[64:65]
	v_pk_mul_f32 v[62:63], v[158:159], v[62:63]
	v_pk_mul_f32 v[60:61], v[160:161], v[60:61]
	v_pk_mul_f32 v[58:59], v[158:159], v[58:59]
	v_pk_mul_f32 v[56:57], v[160:161], v[56:57]
	v_pk_mul_f32 v[54:55], v[158:159], v[54:55]
	v_pk_mul_f32 v[52:53], v[160:161], v[52:53]
	v_pk_mul_f32 v[46:47], v[158:159], v[46:47]
	v_pk_mul_f32 v[44:45], v[160:161], v[44:45]
	v_pk_mul_f32 v[38:39], v[158:159], v[38:39]
	v_pk_mul_f32 v[36:37], v[160:161], v[36:37]
	v_pk_mul_f32 v[30:31], v[158:159], v[30:31]
	v_pk_mul_f32 v[28:29], v[160:161], v[28:29]
	v_pk_mul_f32 v[22:23], v[158:159], v[22:23]
	v_pk_mul_f32 v[20:21], v[160:161], v[20:21]
	v_pk_mul_f32 v[14:15], v[158:159], v[14:15]
	v_pk_mul_f32 v[12:13], v[160:161], v[12:13]
	v_pk_mul_f32 v[50:51], v[158:159], v[50:51]
	v_pk_mul_f32 v[48:49], v[160:161], v[48:49]
	v_pk_mul_f32 v[42:43], v[158:159], v[42:43]
	v_pk_mul_f32 v[40:41], v[160:161], v[40:41]
	v_pk_mul_f32 v[34:35], v[158:159], v[34:35]
	v_pk_mul_f32 v[32:33], v[160:161], v[32:33]
	v_pk_mul_f32 v[26:27], v[158:159], v[26:27]
	v_pk_mul_f32 v[24:25], v[160:161], v[24:25]
	v_pk_mul_f32 v[18:19], v[158:159], v[18:19]
	v_pk_mul_f32 v[16:17], v[160:161], v[16:17]
	v_pk_mul_f32 v[10:11], v[158:159], v[10:11]
	v_pk_mul_f32 v[8:9], v[160:161], v[8:9]
	v_pk_mul_f32 v[6:7], v[158:159], v[6:7]
	v_pk_mul_f32 v[4:5], v[160:161], v[4:5]
	v_pk_mul_f32 v[2:3], v[158:159], v[2:3]
	v_pk_mul_f32 v[0:1], v[160:161], v[0:1]
.LBB0_483:
	s_and_b64 vcc, exec, s[58:59]
	s_cbranch_vccz .LBB0_481
	s_barrier

.LBB0_1309:
	s_cmp_gt_u32 s87, 13
	s_cselect_b64 s[60:61], -1, 0
	s_and_b64 vcc, s[60:61], exec
	s_cselect_b32 s60, -14, 2
	s_add_i32 s60, s60, s87
	s_ashr_i32 s61, s60, 31
	s_lshl_b64 s[60:61], s[60:61], 7
	s_add_u32 s62, s56, s60
	s_addc_u32 s63, s57, s61
	s_add_u32 s76, s54, s60
	s_addc_u32 s77, s55, s61
	s_cmp_gt_u32 s87, 12
	s_cselect_b32 s60, -13, 3
	s_add_i32 s60, s60, s87
	s_ashr_i32 s61, s60, 31
	s_lshl_b64 s[60:61], s[60:61], 7
	s_add_u32 s88, s56, s60
	s_addc_u32 s89, s57, s61
	s_add_u32 s90, s54, s60
	s_mov_b32 s60, s87
	v_add_u32_e32 v150, 0x10000, v136
	v_add_u32_e32 v166, 0x14000, v136
	ds_read_b128 v[138:141], v150
	ds_read_b128 v[142:145], v150 offset:1024
	ds_read_b128 v[146:149], v150 offset:2048
	ds_read_b128 v[150:153], v150 offset:3072
	ds_read_b128 v[154:157], v166
	ds_read_b128 v[158:161], v166 offset:1024
	ds_read_b128 v[162:165], v166 offset:2048
	ds_read_b128 v[166:169], v166 offset:3072
	s_addc_u32 s91, s55, s61
	s_cmp_eq_u32 s87, 14
	s_cselect_b32 s75, s43, s63
	s_cselect_b32 s74, s53, s62
	s_cselect_b32 s77, s47, s77
	s_cselect_b32 s76, s9, s76
	s_cselect_b32 s61, s11, s89
	s_cselect_b32 s60, s10, s88
	s_cselect_b32 s63, s86, s91
	s_cselect_b32 s62, s12, s90
	ds_read_b128 v[170:173], v137
	ds_read_b128 v[174:177], v137 offset:1024
	ds_read_b128 v[178:181], v137 offset:2048
	ds_read_b128 v[182:185], v137 offset:3072
	ds_read_b128 v[190:193], v137 offset:4096
	ds_read_b128 v[194:197], v137 offset:5120
	ds_read_b128 v[198:201], v137 offset:6144
	ds_read_b128 v[202:205], v137 offset:7168
	s_add_u32 s88, s58, 0x40080
	s_addc_u32 s89, s59, 0
	s_mov_b32 m0, s82
	s_nop 0
	global_load_lds_dwordx4 v132, s[88:89]
	s_add_i32 s90, s34, 0xe000
	s_mov_b32 m0, s90
	s_nop 0
	global_load_lds_dwordx4 v134, s[88:89]
	s_setprio 1
	s_waitcnt vmcnt(8)
	s_waitcnt lgkmcnt(0)
	s_barrier
	v_mfma_i32_16x16x64_i8 v[124:127], v[138:141], v[170:173], v[124:127]
	v_mfma_i32_16x16x64_i8 v[120:123], v[146:149], v[170:173], v[120:123]
	v_mfma_i32_16x16x64_i8 v[116:119], v[138:141], v[178:181], v[116:119]
	v_mfma_i32_16x16x64_i8 v[112:115], v[146:149], v[178:181], v[112:115]
	v_mfma_i32_16x16x64_i8 v[108:111], v[138:141], v[190:193], v[108:111]
	v_mfma_i32_16x16x64_i8 v[104:107], v[146:149], v[190:193], v[104:107]
	v_mfma_i32_16x16x64_i8 v[100:103], v[138:141], v[198:201], v[100:103]
	v_mfma_i32_16x16x64_i8 v[96:99], v[146:149], v[198:201], v[96:99]
	v_mfma_i32_16x16x64_i8 v[124:127], v[142:145], v[174:177], v[124:127]
	v_mfma_i32_16x16x64_i8 v[120:123], v[150:153], v[174:177], v[120:123]
	v_mfma_i32_16x16x64_i8 v[116:119], v[142:145], v[182:185], v[116:119]
	v_mfma_i32_16x16x64_i8 v[112:115], v[150:153], v[182:185], v[112:115]
	v_mfma_i32_16x16x64_i8 v[108:111], v[142:145], v[194:197], v[108:111]
	v_mfma_i32_16x16x64_i8 v[104:107], v[150:153], v[194:197], v[104:107]
	v_mfma_i32_16x16x64_i8 v[100:103], v[142:145], v[202:205], v[100:103]
	v_mfma_i32_16x16x64_i8 v[96:99], v[150:153], v[202:205], v[96:99]
	v_mfma_i32_16x16x64_i8 v[92:95], v[154:157], v[170:173], v[92:95]
	v_mfma_i32_16x16x64_i8 v[88:91], v[162:165], v[170:173], v[88:91]
	v_mfma_i32_16x16x64_i8 v[84:87], v[154:157], v[178:181], v[84:87]
	v_mfma_i32_16x16x64_i8 v[80:83], v[162:165], v[178:181], v[80:83]
	v_mfma_i32_16x16x64_i8 v[76:79], v[154:157], v[190:193], v[76:79]
	v_mfma_i32_16x16x64_i8 v[72:75], v[162:165], v[190:193], v[72:75]
	v_mfma_i32_16x16x64_i8 v[68:71], v[154:157], v[198:201], v[68:71]
	v_mfma_i32_16x16x64_i8 v[64:67], v[162:165], v[198:201], v[64:67]
	v_mfma_i32_16x16x64_i8 v[92:95], v[158:161], v[174:177], v[92:95]
	v_mfma_i32_16x16x64_i8 v[88:91], v[166:169], v[174:177], v[88:91]
	v_mfma_i32_16x16x64_i8 v[84:87], v[158:161], v[182:185], v[84:87]
	v_mfma_i32_16x16x64_i8 v[80:83], v[166:169], v[182:185], v[80:83]
	v_mfma_i32_16x16x64_i8 v[76:79], v[158:161], v[194:197], v[76:79]
	v_mfma_i32_16x16x64_i8 v[72:75], v[166:169], v[194:197], v[72:75]
	v_mfma_i32_16x16x64_i8 v[68:71], v[158:161], v[202:205], v[68:71]
	v_mfma_i32_16x16x64_i8 v[64:67], v[166:169], v[202:205], v[64:67]
	s_barrier
	s_setprio 0
	ds_read_b128 v[170:173], v137 offset:16384
	ds_read_b128 v[174:177], v137 offset:17408
	ds_read_b128 v[178:181], v137 offset:18432
	ds_read_b128 v[182:185], v137 offset:19456
	ds_read_b128 v[190:193], v137 offset:20480
	ds_read_b128 v[194:197], v137 offset:21504
	ds_read_b128 v[198:201], v137 offset:22528
	ds_read_b128 v[202:205], v137 offset:23552
	s_mov_b32 m0, s35
	s_nop 0
	global_load_lds_dwordx4 v133, s[76:77]
	s_nop 0
	s_mov_b32 m0, s36
	s_nop 0
	global_load_lds_dwordx4 v135, s[76:77]
	s_add_u32 s76, s76, 0x40000
	s_addc_u32 s77, s77, 0
	s_mov_b32 m0, s37
	s_nop 0
	global_load_lds_dwordx4 v133, s[76:77]
	s_nop 0
	s_mov_b32 m0, s65
	s_nop 0
	global_load_lds_dwordx4 v135, s[76:77]
	s_mov_b32 m0, s34
	s_nop 0
	global_load_lds_dwordx4 v132, s[74:75]
	s_nop 0
	s_mov_b32 m0, s66
	s_nop 0
	global_load_lds_dwordx4 v134, s[74:75]
	s_setprio 1
	s_waitcnt vmcnt(8)
	s_waitcnt lgkmcnt(0)
	s_barrier
	v_mfma_i32_16x16x64_i8 v[60:63], v[138:141], v[170:173], v[60:63]
	v_mfma_i32_16x16x64_i8 v[56:59], v[146:149], v[170:173], v[56:59]
	v_mfma_i32_16x16x64_i8 v[52:55], v[138:141], v[178:181], v[52:55]
	v_mfma_i32_16x16x64_i8 v[48:51], v[146:149], v[178:181], v[48:51]
	v_mfma_i32_16x16x64_i8 v[44:47], v[138:141], v[190:193], v[44:47]
	v_mfma_i32_16x16x64_i8 v[40:43], v[146:149], v[190:193], v[40:43]
	v_mfma_i32_16x16x64_i8 v[36:39], v[138:141], v[198:201], v[36:39]
	v_mfma_i32_16x16x64_i8 v[32:35], v[146:149], v[198:201], v[32:35]
	v_mfma_i32_16x16x64_i8 v[60:63], v[142:145], v[174:177], v[60:63]
	v_mfma_i32_16x16x64_i8 v[56:59], v[150:153], v[174:177], v[56:59]
	v_mfma_i32_16x16x64_i8 v[52:55], v[142:145], v[182:185], v[52:55]
	v_mfma_i32_16x16x64_i8 v[48:51], v[150:153], v[182:185], v[48:51]
	v_mfma_i32_16x16x64_i8 v[44:47], v[142:145], v[194:197], v[44:47]
	v_mfma_i32_16x16x64_i8 v[40:43], v[150:153], v[194:197], v[40:43]
	v_mfma_i32_16x16x64_i8 v[36:39], v[142:145], v[202:205], v[36:39]
	v_mfma_i32_16x16x64_i8 v[32:35], v[150:153], v[202:205], v[32:35]
	v_mfma_i32_16x16x64_i8 v[28:31], v[154:157], v[170:173], v[28:31]
	v_mfma_i32_16x16x64_i8 v[24:27], v[162:165], v[170:173], v[24:27]
	v_mfma_i32_16x16x64_i8 v[20:23], v[154:157], v[178:181], v[20:23]
	v_mfma_i32_16x16x64_i8 v[16:19], v[162:165], v[178:181], v[16:19]
	v_mfma_i32_16x16x64_i8 v[12:15], v[154:157], v[190:193], v[12:15]
	v_mfma_i32_16x16x64_i8 v[8:11], v[162:165], v[190:193], v[8:11]
	v_mfma_i32_16x16x64_i8 v[4:7], v[154:157], v[198:201], v[4:7]
	v_mfma_i32_16x16x64_i8 v[0:3], v[162:165], v[198:201], v[0:3]
	v_mfma_i32_16x16x64_i8 v[28:31], v[158:161], v[174:177], v[28:31]
	v_mfma_i32_16x16x64_i8 v[24:27], v[166:169], v[174:177], v[24:27]
	v_mfma_i32_16x16x64_i8 v[20:23], v[158:161], v[182:185], v[20:23]
	v_mfma_i32_16x16x64_i8 v[16:19], v[166:169], v[182:185], v[16:19]
	v_mfma_i32_16x16x64_i8 v[12:15], v[158:161], v[194:197], v[12:15]
	v_mfma_i32_16x16x64_i8 v[8:11], v[166:169], v[194:197], v[8:11]
	v_mfma_i32_16x16x64_i8 v[4:7], v[158:161], v[202:205], v[4:7]
	v_mfma_i32_16x16x64_i8 v[0:3], v[166:169], v[202:205], v[0:3]
	s_barrier
	s_setprio 0
	v_add_u32_e32 v150, 0x18000, v136
	v_add_u32_e32 v166, 0x1c000, v136
	ds_read_b128 v[138:141], v150
	ds_read_b128 v[142:145], v150 offset:1024
	ds_read_b128 v[146:149], v150 offset:2048
	ds_read_b128 v[150:153], v150 offset:3072
	ds_read_b128 v[154:157], v166
	ds_read_b128 v[158:161], v166 offset:1024
	ds_read_b128 v[162:165], v166 offset:2048
	ds_read_b128 v[166:169], v166 offset:3072
	ds_read_b128 v[170:173], v137 offset:32768
	ds_read_b128 v[174:177], v137 offset:33792
	ds_read_b128 v[178:181], v137 offset:34816
	ds_read_b128 v[182:185], v137 offset:35840
	ds_read_b128 v[190:193], v137 offset:36864
	ds_read_b128 v[194:197], v137 offset:37888
	ds_read_b128 v[198:201], v137 offset:38912
	ds_read_b128 v[202:205], v137 offset:39936
	s_add_u32 s74, s74, 0x40000
	s_addc_u32 s75, s75, 0
	s_mov_b32 m0, s67
	s_nop 0
	global_load_lds_dwordx4 v132, s[74:75]
	s_nop 0
	s_mov_b32 m0, s68
	s_nop 0
	global_load_lds_dwordx4 v134, s[74:75]
	s_setprio 1
	s_waitcnt vmcnt(8)
	s_waitcnt lgkmcnt(0)
	s_barrier
	v_mfma_i32_16x16x64_i8 v[124:127], v[138:141], v[170:173], v[124:127]
	v_mfma_i32_16x16x64_i8 v[120:123], v[146:149], v[170:173], v[120:123]
	v_mfma_i32_16x16x64_i8 v[116:119], v[138:141], v[178:181], v[116:119]
	v_mfma_i32_16x16x64_i8 v[112:115], v[146:149], v[178:181], v[112:115]
	v_mfma_i32_16x16x64_i8 v[108:111], v[138:141], v[190:193], v[108:111]
	v_mfma_i32_16x16x64_i8 v[104:107], v[146:149], v[190:193], v[104:107]
	v_mfma_i32_16x16x64_i8 v[100:103], v[138:141], v[198:201], v[100:103]
	v_mfma_i32_16x16x64_i8 v[96:99], v[146:149], v[198:201], v[96:99]
	v_mfma_i32_16x16x64_i8 v[124:127], v[142:145], v[174:177], v[124:127]
	v_mfma_i32_16x16x64_i8 v[120:123], v[150:153], v[174:177], v[120:123]
	v_mfma_i32_16x16x64_i8 v[116:119], v[142:145], v[182:185], v[116:119]
	v_mfma_i32_16x16x64_i8 v[112:115], v[150:153], v[182:185], v[112:115]
	v_mfma_i32_16x16x64_i8 v[108:111], v[142:145], v[194:197], v[108:111]
	v_mfma_i32_16x16x64_i8 v[104:107], v[150:153], v[194:197], v[104:107]
	v_mfma_i32_16x16x64_i8 v[100:103], v[142:145], v[202:205], v[100:103]
	v_mfma_i32_16x16x64_i8 v[96:99], v[150:153], v[202:205], v[96:99]
	v_mfma_i32_16x16x64_i8 v[92:95], v[154:157], v[170:173], v[92:95]
	v_mfma_i32_16x16x64_i8 v[88:91], v[162:165], v[170:173], v[88:91]
	v_mfma_i32_16x16x64_i8 v[84:87], v[154:157], v[178:181], v[84:87]
	v_mfma_i32_16x16x64_i8 v[80:83], v[162:165], v[178:181], v[80:83]
	v_mfma_i32_16x16x64_i8 v[76:79], v[154:157], v[190:193], v[76:79]
	v_mfma_i32_16x16x64_i8 v[72:75], v[162:165], v[190:193], v[72:75]
	v_mfma_i32_16x16x64_i8 v[68:71], v[154:157], v[198:201], v[68:71]
	v_mfma_i32_16x16x64_i8 v[64:67], v[162:165], v[198:201], v[64:67]
	v_mfma_i32_16x16x64_i8 v[92:95], v[158:161], v[174:177], v[92:95]
	v_mfma_i32_16x16x64_i8 v[88:91], v[166:169], v[174:177], v[88:91]
	v_mfma_i32_16x16x64_i8 v[84:87], v[158:161], v[182:185], v[84:87]
	v_mfma_i32_16x16x64_i8 v[80:83], v[166:169], v[182:185], v[80:83]
	v_mfma_i32_16x16x64_i8 v[76:79], v[158:161], v[194:197], v[76:79]
	v_mfma_i32_16x16x64_i8 v[72:75], v[166:169], v[194:197], v[72:75]
	v_mfma_i32_16x16x64_i8 v[68:71], v[158:161], v[202:205], v[68:71]
	v_mfma_i32_16x16x64_i8 v[64:67], v[166:169], v[202:205], v[64:67]
	s_barrier
	s_setprio 0
	ds_read_b128 v[170:173], v137 offset:49152
	ds_read_b128 v[174:177], v137 offset:50176
	ds_read_b128 v[178:181], v137 offset:51200
	ds_read_b128 v[182:185], v137 offset:52224
	ds_read_b128 v[190:193], v137 offset:53248
	ds_read_b128 v[194:197], v137 offset:54272
	ds_read_b128 v[198:201], v137 offset:55296
	ds_read_b128 v[202:205], v137 offset:56320
	s_mov_b32 m0, s71
	s_nop 0
	global_load_lds_dwordx4 v133, s[62:63]
	s_nop 0
	s_mov_b32 m0, s72
	s_nop 0
	global_load_lds_dwordx4 v135, s[62:63]
	s_add_u32 s62, s62, 0x40000
	s_addc_u32 s63, s63, 0
	s_mov_b32 m0, s80
	s_nop 0
	global_load_lds_dwordx4 v133, s[62:63]
	s_nop 0
	s_mov_b32 m0, s81
	s_nop 0
	global_load_lds_dwordx4 v135, s[62:63]
	s_mov_b32 m0, s78
	s_nop 0
	global_load_lds_dwordx4 v132, s[60:61]
	s_nop 0
	s_mov_b32 m0, s79
	s_nop 0
	global_load_lds_dwordx4 v134, s[60:61]
	s_setprio 1
	s_waitcnt vmcnt(8)
	s_waitcnt lgkmcnt(0)
	s_barrier
	v_mfma_i32_16x16x64_i8 v[60:63], v[138:141], v[170:173], v[60:63]
	v_mfma_i32_16x16x64_i8 v[56:59], v[146:149], v[170:173], v[56:59]
	v_mfma_i32_16x16x64_i8 v[52:55], v[138:141], v[178:181], v[52:55]
	v_mfma_i32_16x16x64_i8 v[48:51], v[146:149], v[178:181], v[48:51]
	v_mfma_i32_16x16x64_i8 v[44:47], v[138:141], v[190:193], v[44:47]
	v_mfma_i32_16x16x64_i8 v[40:43], v[146:149], v[190:193], v[40:43]
	v_mfma_i32_16x16x64_i8 v[36:39], v[138:141], v[198:201], v[36:39]
	v_mfma_i32_16x16x64_i8 v[32:35], v[146:149], v[198:201], v[32:35]
	v_mfma_i32_16x16x64_i8 v[60:63], v[142:145], v[174:177], v[60:63]
	v_mfma_i32_16x16x64_i8 v[56:59], v[150:153], v[174:177], v[56:59]
	v_mfma_i32_16x16x64_i8 v[52:55], v[142:145], v[182:185], v[52:55]
	v_mfma_i32_16x16x64_i8 v[48:51], v[150:153], v[182:185], v[48:51]
	v_mfma_i32_16x16x64_i8 v[44:47], v[142:145], v[194:197], v[44:47]
	v_mfma_i32_16x16x64_i8 v[40:43], v[150:153], v[194:197], v[40:43]
	v_mfma_i32_16x16x64_i8 v[36:39], v[142:145], v[202:205], v[36:39]
	v_mfma_i32_16x16x64_i8 v[32:35], v[150:153], v[202:205], v[32:35]
	v_mfma_i32_16x16x64_i8 v[28:31], v[154:157], v[170:173], v[28:31]
	v_mfma_i32_16x16x64_i8 v[24:27], v[162:165], v[170:173], v[24:27]
	v_mfma_i32_16x16x64_i8 v[20:23], v[154:157], v[178:181], v[20:23]
	v_mfma_i32_16x16x64_i8 v[16:19], v[162:165], v[178:181], v[16:19]
	v_mfma_i32_16x16x64_i8 v[12:15], v[154:157], v[190:193], v[12:15]
	v_mfma_i32_16x16x64_i8 v[8:11], v[162:165], v[190:193], v[8:11]
	v_mfma_i32_16x16x64_i8 v[4:7], v[154:157], v[198:201], v[4:7]
	v_mfma_i32_16x16x64_i8 v[0:3], v[162:165], v[198:201], v[0:3]
	v_mfma_i32_16x16x64_i8 v[28:31], v[158:161], v[174:177], v[28:31]
	v_mfma_i32_16x16x64_i8 v[24:27], v[166:169], v[174:177], v[24:27]
	v_mfma_i32_16x16x64_i8 v[20:23], v[158:161], v[182:185], v[20:23]
	v_mfma_i32_16x16x64_i8 v[16:19], v[166:169], v[182:185], v[16:19]
	v_mfma_i32_16x16x64_i8 v[12:15], v[158:161], v[194:197], v[12:15]
	v_mfma_i32_16x16x64_i8 v[8:11], v[166:169], v[194:197], v[8:11]
	v_mfma_i32_16x16x64_i8 v[4:7], v[158:161], v[202:205], v[4:7]
	v_mfma_i32_16x16x64_i8 v[0:3], v[166:169], v[202:205], v[0:3]
	s_barrier
	s_setprio 0
	s_add_i32 s87, s87, 2
	s_add_u32 s58, s58, 0x100
	s_addc_u32 s59, s59, 0
	s_cbranch_vccz .LBB0_1309
	v_cvt_f32_i32_e32 v124, v124
	v_cvt_f32_i32_e32 v125, v125
	v_cvt_f32_i32_e32 v140, v88
	v_cvt_f32_i32_e32 v88, v86
	v_cvt_f32_i32_e32 v86, v80
	v_cvt_f32_i32_e32 v80, v78
	v_cvt_f32_i32_e32 v78, v72
	v_cvt_f32_i32_e32 v72, v70
	v_cvt_f32_i32_e32 v70, v64
	v_cvt_f32_i32_e32 v64, v60
	v_cvt_f32_i32_e32 v60, v56
	v_cvt_f32_i32_e32 v56, v52
	v_cvt_f32_i32_e32 v52, v48
	v_cvt_f32_i32_e32 v48, v44
	v_cvt_f32_i32_e32 v44, v40
	v_cvt_f32_i32_e32 v40, v36
	v_cvt_f32_i32_e32 v36, v32
	v_cvt_f32_i32_e32 v32, v34
	v_cvt_f32_i32_e32 v34, v30
	v_cvt_f32_i32_e32 v30, v24
	v_cvt_f32_i32_e32 v24, v22
	v_cvt_f32_i32_e32 v22, v16
	v_cvt_f32_i32_e32 v16, v14
	v_cvt_f32_i32_e32 v14, v8
	v_cvt_f32_i32_e32 v8, v4
	v_cvt_f32_i32_e32 v4, v0
	v_mbcnt_lo_u32_b32 v0, -1, 0
	v_mbcnt_hi_u32_b32 v0, -1, v0
	s_lshl_b32 s9, s52, 8
	v_cvt_f32_i32_e32 v141, v89
	v_cvt_f32_i32_e32 v89, v87
	v_cvt_f32_i32_e32 v87, v81
	v_cvt_f32_i32_e32 v81, v79
	v_cvt_f32_i32_e32 v79, v73
	v_cvt_f32_i32_e32 v73, v71
	v_cvt_f32_i32_e32 v71, v65
	v_cvt_f32_i32_e32 v65, v61
	v_cvt_f32_i32_e32 v61, v57
	v_cvt_f32_i32_e32 v57, v53
	v_cvt_f32_i32_e32 v53, v49
	v_cvt_f32_i32_e32 v49, v45
	v_cvt_f32_i32_e32 v45, v41
	v_cvt_f32_i32_e32 v41, v37
	v_cvt_f32_i32_e32 v37, v33
	v_cvt_f32_i32_e32 v33, v35
	v_cvt_f32_i32_e32 v35, v31
	v_cvt_f32_i32_e32 v31, v25
	v_cvt_f32_i32_e32 v25, v23
	v_cvt_f32_i32_e32 v23, v17
	v_cvt_f32_i32_e32 v17, v15
	v_cvt_f32_i32_e32 v15, v9
	v_cvt_f32_i32_e32 v9, v5
	v_cvt_f32_i32_e32 v5, v1
	s_add_i32 s9, s9, s69
	v_ashrrev_i32_e32 v1, 2, v0
	v_cvt_f32_i32_e32 v139, v121
	v_cvt_f32_i32_e32 v121, v117
	v_cvt_f32_i32_e32 v117, v113
	v_cvt_f32_i32_e32 v113, v109
	v_cvt_f32_i32_e32 v109, v105
	v_cvt_f32_i32_e32 v105, v101
	v_cvt_f32_i32_e32 v101, v97
	v_cvt_f32_i32_e32 v97, v99
	v_cvt_f32_i32_e32 v99, v93
	v_cvt_f32_i32_e32 v142, v90
	v_cvt_f32_i32_e32 v90, v84
	v_cvt_f32_i32_e32 v84, v82
	v_cvt_f32_i32_e32 v82, v76
	v_cvt_f32_i32_e32 v76, v74
	v_cvt_f32_i32_e32 v74, v68
	v_cvt_f32_i32_e32 v68, v66
	v_cvt_f32_i32_e32 v66, v28
	v_cvt_f32_i32_e32 v28, v26
	v_cvt_f32_i32_e32 v26, v20
	v_cvt_f32_i32_e32 v20, v18
	v_cvt_f32_i32_e32 v18, v12
	v_cvt_f32_i32_e32 v12, v10
	v_and_b32_e32 v10, 3, v0
	v_and_b32_e32 v0, -4, v0
	v_add_u32_e32 v93, s9, v1
	s_lshl_b32 s9, s85, 7
	v_cvt_f32_i32_e32 v138, v120
	v_cvt_f32_i32_e32 v120, v116
	v_cvt_f32_i32_e32 v116, v112
	v_cvt_f32_i32_e32 v112, v108
	v_cvt_f32_i32_e32 v108, v104
	v_cvt_f32_i32_e32 v104, v100
	v_cvt_f32_i32_e32 v100, v96
	v_cvt_f32_i32_e32 v96, v98
	v_cvt_f32_i32_e32 v98, v92
	v_cvt_f32_i32_e32 v143, v91
	v_cvt_f32_i32_e32 v91, v85
	v_cvt_f32_i32_e32 v85, v83
	v_cvt_f32_i32_e32 v83, v77
	v_cvt_f32_i32_e32 v77, v75
	v_cvt_f32_i32_e32 v75, v69
	v_cvt_f32_i32_e32 v69, v67
	v_cvt_f32_i32_e32 v67, v29
	v_cvt_f32_i32_e32 v29, v27
	v_cvt_f32_i32_e32 v27, v21
	v_cvt_f32_i32_e32 v21, v19
	v_cvt_f32_i32_e32 v19, v13
	v_cvt_f32_i32_e32 v13, v11
	v_lshl_add_u32 v92, v10, 6, v0
	v_lshl_or_b32 v0, v10, 3, s9
	s_and_b64 vcc, exec, s[40:41]
	s_cbranch_vccz .LBB0_1312
	s_barrier
.LBB0_1312:
	v_pk_mul_f32 v[10:11], v[128:129], v[124:125]
	v_cvt_f32_i32_e32 v126, v126
	v_exp_f32_e32 v10, v10
	v_exp_f32_e32 v11, v11
	v_cvt_f32_i32_e32 v127, v127
	v_pk_mul_f32 v[124:125], v[130:131], v[124:125]
	v_cvt_f32_i32_e32 v94, v94
	v_pk_add_f32 v[10:11], v[10:11], 1.0 op_sel_hi:[1,0]
	v_pk_mul_f32 v[98:99], v[124:125], v[98:99]
	v_rcp_f32_e32 v10, v10
	v_rcp_f32_e32 v11, v11
	v_cvt_f32_i32_e32 v95, v95
	v_pk_mul_f32 v[124:125], v[130:131], v[126:127]
	v_cvt_f32_i32_e32 v122, v122
	v_pk_mul_f32 v[10:11], v[10:11], v[98:99]
	v_pk_mul_f32 v[98:99], v[128:129], v[126:127]
	v_pk_mul_f32 v[94:95], v[124:125], v[94:95]
	v_exp_f32_e32 v98, v98
	v_exp_f32_e32 v99, v99
	v_cvt_f32_i32_e32 v123, v123
	v_pk_mul_f32 v[124:125], v[130:131], v[138:139]
	v_or_b32_e32 v0, s70, v0
	v_pk_add_f32 v[98:99], v[98:99], 1.0 op_sel_hi:[1,0]
	v_pk_mul_f32 v[124:125], v[124:125], v[140:141]
	v_rcp_f32_e32 v98, v98
	v_rcp_f32_e32 v99, v99
	s_movk_i32 s9, 0x1c00
	v_ashrrev_i32_e32 v1, 31, v0
	v_cvt_f32_i32_e32 v118, v118
	v_pk_mul_f32 v[94:95], v[98:99], v[94:95]
	v_pk_mul_f32 v[98:99], v[128:129], v[138:139]
	v_cvt_f32_i32_e32 v119, v119
	v_exp_f32_e32 v98, v98
	v_exp_f32_e32 v99, v99
	v_cvt_f32_i32_e32 v114, v114
	v_cvt_f32_i32_e32 v115, v115
	v_cvt_f32_i32_e32 v110, v110
	v_pk_add_f32 v[98:99], v[98:99], 1.0 op_sel_hi:[1,0]
	v_cvt_f32_i32_e32 v111, v111
	v_rcp_f32_e32 v98, v98
	v_rcp_f32_e32 v99, v99
	v_cvt_f32_i32_e32 v106, v106
	v_cvt_f32_i32_e32 v107, v107
	v_cvt_f32_i32_e32 v102, v102
	v_pk_mul_f32 v[98:99], v[98:99], v[124:125]
	v_pk_mul_f32 v[124:125], v[128:129], v[122:123]
	v_pk_mul_f32 v[122:123], v[130:131], v[122:123]
	v_exp_f32_e32 v124, v124
	v_exp_f32_e32 v125, v125
	v_pk_mul_f32 v[122:123], v[122:123], v[142:143]
	v_cvt_f32_i32_e32 v103, v103
	v_cvt_f32_i32_e32 v62, v62
	v_pk_add_f32 v[124:125], v[124:125], 1.0 op_sel_hi:[1,0]
	v_cvt_f32_i32_e32 v63, v63
	v_rcp_f32_e32 v124, v124
	v_rcp_f32_e32 v125, v125
	v_cvt_f32_i32_e32 v58, v58
	v_cvt_f32_i32_e32 v59, v59
	v_cvt_f32_i32_e32 v54, v54
	v_pk_mul_f32 v[122:123], v[124:125], v[122:123]
	v_cvt_pk_fp8_f32 v124, v10, v11
	v_cvt_pk_fp8_f32 v10, v98, v99
	v_cvt_f32_i32_e32 v55, v55
	v_cvt_pk_fp8_f32 v124, v94, v95 op_sel:[0,0,1]
	v_cvt_f32_i32_e32 v50, v50
	v_cvt_pk_fp8_f32 v10, v122, v123 op_sel:[0,0,1]
	v_cvt_f32_i32_e32 v51, v51
	ds_bpermute_b32 v94, v92, v124
	v_cvt_f32_i32_e32 v46, v46
	ds_bpermute_b32 v95, v92, v10
	v_mov_b64_e32 v[10:11], s[22:23]
	v_mad_i64_i32 v[98:99], s[10:11], v93, s9, v[10:11]
	v_lshl_add_u64 v[98:99], v[98:99], 0, v[0:1]
	s_waitcnt lgkmcnt(0)
	global_store_dwordx2 v[98:99], v[94:95], off
	v_pk_mul_f32 v[94:95], v[128:129], v[120:121]
	v_pk_mul_f32 v[98:99], v[130:131], v[120:121]
	v_exp_f32_e32 v94, v94
	v_exp_f32_e32 v95, v95
	v_pk_mul_f32 v[90:91], v[98:99], v[90:91]
	v_pk_mul_f32 v[98:99], v[130:131], v[118:119]
	v_cvt_f32_i32_e32 v47, v47
	v_pk_add_f32 v[94:95], v[94:95], 1.0 op_sel_hi:[1,0]
	v_pk_mul_f32 v[88:89], v[98:99], v[88:89]
	v_rcp_f32_e32 v94, v94
	v_rcp_f32_e32 v95, v95
	v_pk_mul_f32 v[98:99], v[130:131], v[116:117]
	v_cvt_f32_i32_e32 v42, v42
	v_pk_mul_f32 v[86:87], v[98:99], v[86:87]
	v_pk_mul_f32 v[90:91], v[94:95], v[90:91]
	v_pk_mul_f32 v[94:95], v[128:129], v[118:119]
	v_pk_mul_f32 v[98:99], v[130:131], v[114:115]
	v_exp_f32_e32 v94, v94
	v_exp_f32_e32 v95, v95
	v_pk_mul_f32 v[84:85], v[98:99], v[84:85]
	v_cvt_f32_i32_e32 v43, v43
	v_cvt_f32_i32_e32 v38, v38
	v_pk_add_f32 v[94:95], v[94:95], 1.0 op_sel_hi:[1,0]
	v_cvt_f32_i32_e32 v39, v39
	v_rcp_f32_e32 v94, v94
	v_rcp_f32_e32 v95, v95
	v_cvt_f32_i32_e32 v6, v6
	v_cvt_f32_i32_e32 v7, v7
	v_cvt_f32_i32_e32 v2, v2
	v_pk_mul_f32 v[88:89], v[94:95], v[88:89]
	v_pk_mul_f32 v[94:95], v[128:129], v[116:117]
	v_cvt_f32_i32_e32 v3, v3
	v_exp_f32_e32 v94, v94
	v_exp_f32_e32 v95, v95
	s_mov_b64 s[52:53], -1
	s_andn2_b64 vcc, exec, s[44:45]
	v_readlane_b32 s90, v255, 39
	v_pk_add_f32 v[94:95], v[94:95], 1.0 op_sel_hi:[1,0]
	v_readlane_b32 s91, v255, 40
	v_rcp_f32_e32 v94, v94
	v_rcp_f32_e32 v95, v95
	s_nop 0
	v_pk_mul_f32 v[86:87], v[94:95], v[86:87]
	v_pk_mul_f32 v[94:95], v[128:129], v[114:115]
	s_nop 0
	v_exp_f32_e32 v94, v94
	v_exp_f32_e32 v95, v95
	s_nop 0
	v_pk_add_f32 v[94:95], v[94:95], 1.0 op_sel_hi:[1,0]
	s_nop 0
	v_rcp_f32_e32 v94, v94
	v_rcp_f32_e32 v95, v95
	s_nop 0
	v_pk_mul_f32 v[84:85], v[94:95], v[84:85]
	v_cvt_pk_fp8_f32 v94, v90, v91
	v_cvt_pk_fp8_f32 v94, v88, v89 op_sel:[0,0,1]
	v_cvt_pk_fp8_f32 v89, v86, v87
	v_pk_mul_f32 v[86:87], v[130:131], v[112:113]
	ds_bpermute_b32 v88, v92, v94
	v_pk_mul_f32 v[82:83], v[86:87], v[82:83]
	v_cvt_pk_fp8_f32 v89, v84, v85 op_sel:[0,0,1]
	v_add_u32_e32 v84, 16, v93
	v_mad_i64_i32 v[84:85], s[10:11], v84, s9, v[10:11]
	ds_bpermute_b32 v89, v92, v89
	v_lshl_add_u64 v[84:85], v[84:85], 0, v[0:1]
	v_pk_mul_f32 v[86:87], v[130:131], v[110:111]
	s_waitcnt lgkmcnt(0)
	global_store_dwordx2 v[84:85], v[88:89], off
	v_pk_mul_f32 v[84:85], v[128:129], v[112:113]
	v_pk_mul_f32 v[80:81], v[86:87], v[80:81]
	v_exp_f32_e32 v84, v84
	v_exp_f32_e32 v85, v85
	v_pk_mul_f32 v[86:87], v[130:131], v[108:109]
	v_pk_add_f32 v[84:85], v[84:85], 1.0 op_sel_hi:[1,0]
	s_nop 0
	v_rcp_f32_e32 v84, v84
	v_rcp_f32_e32 v85, v85
	v_pk_mul_f32 v[78:79], v[86:87], v[78:79]
	v_pk_mul_f32 v[86:87], v[130:131], v[106:107]
	v_pk_mul_f32 v[82:83], v[84:85], v[82:83]
	v_pk_mul_f32 v[84:85], v[128:129], v[110:111]
	v_pk_mul_f32 v[76:77], v[86:87], v[76:77]
	v_exp_f32_e32 v84, v84
	v_exp_f32_e32 v85, v85
	s_nop 0
	v_pk_add_f32 v[84:85], v[84:85], 1.0 op_sel_hi:[1,0]
	s_nop 0
	v_rcp_f32_e32 v84, v84
	v_rcp_f32_e32 v85, v85
	s_nop 0
	v_pk_mul_f32 v[80:81], v[84:85], v[80:81]
	v_pk_mul_f32 v[84:85], v[128:129], v[108:109]
	s_nop 0
	v_exp_f32_e32 v84, v84
	v_exp_f32_e32 v85, v85
	s_nop 0
	v_pk_add_f32 v[84:85], v[84:85], 1.0 op_sel_hi:[1,0]
	s_nop 0
	v_rcp_f32_e32 v84, v84
	v_rcp_f32_e32 v85, v85
	s_nop 0
	v_pk_mul_f32 v[78:79], v[84:85], v[78:79]
	v_pk_mul_f32 v[84:85], v[128:129], v[106:107]
	s_nop 0
	v_exp_f32_e32 v84, v84
	v_exp_f32_e32 v85, v85
	s_nop 0
	v_pk_add_f32 v[84:85], v[84:85], 1.0 op_sel_hi:[1,0]
	s_nop 0
	v_rcp_f32_e32 v84, v84
	v_rcp_f32_e32 v85, v85
	s_nop 0
	v_pk_mul_f32 v[76:77], v[84:85], v[76:77]
	v_cvt_pk_fp8_f32 v84, v82, v83
	v_cvt_pk_fp8_f32 v84, v80, v81 op_sel:[0,0,1]
	v_cvt_pk_fp8_f32 v81, v78, v79
	v_pk_mul_f32 v[78:79], v[130:131], v[104:105]
	ds_bpermute_b32 v80, v92, v84
	v_pk_mul_f32 v[74:75], v[78:79], v[74:75]
	v_cvt_pk_fp8_f32 v81, v76, v77 op_sel:[0,0,1]
	v_add_u32_e32 v76, 32, v93
	v_mad_i64_i32 v[76:77], s[10:11], v76, s9, v[10:11]
	ds_bpermute_b32 v81, v92, v81
	v_lshl_add_u64 v[76:77], v[76:77], 0, v[0:1]
	v_pk_mul_f32 v[78:79], v[130:131], v[102:103]
	s_waitcnt lgkmcnt(0)
	global_store_dwordx2 v[76:77], v[80:81], off
	v_pk_mul_f32 v[76:77], v[128:129], v[104:105]
	v_pk_mul_f32 v[72:73], v[78:79], v[72:73]
	v_exp_f32_e32 v76, v76
	v_exp_f32_e32 v77, v77
	v_pk_mul_f32 v[78:79], v[130:131], v[100:101]
	v_pk_add_f32 v[76:77], v[76:77], 1.0 op_sel_hi:[1,0]
	s_nop 0
	v_rcp_f32_e32 v76, v76
	v_rcp_f32_e32 v77, v77
	v_pk_mul_f32 v[70:71], v[78:79], v[70:71]
	v_pk_mul_f32 v[78:79], v[130:131], v[96:97]
	v_pk_mul_f32 v[74:75], v[76:77], v[74:75]
	v_pk_mul_f32 v[76:77], v[128:129], v[102:103]
	v_pk_mul_f32 v[68:69], v[78:79], v[68:69]
	v_exp_f32_e32 v76, v76
	v_exp_f32_e32 v77, v77
	s_nop 0
	v_pk_add_f32 v[76:77], v[76:77], 1.0 op_sel_hi:[1,0]
	s_nop 0
	v_rcp_f32_e32 v76, v76
	v_rcp_f32_e32 v77, v77
	s_nop 0
	v_pk_mul_f32 v[72:73], v[76:77], v[72:73]
	v_pk_mul_f32 v[76:77], v[128:129], v[100:101]
	s_nop 0
	v_exp_f32_e32 v76, v76
	v_exp_f32_e32 v77, v77
	s_nop 0
	v_pk_add_f32 v[76:77], v[76:77], 1.0 op_sel_hi:[1,0]
	s_nop 0
	v_rcp_f32_e32 v76, v76
	v_rcp_f32_e32 v77, v77
	s_nop 0
	v_pk_mul_f32 v[70:71], v[76:77], v[70:71]
	v_pk_mul_f32 v[76:77], v[128:129], v[96:97]
	s_nop 0
	v_exp_f32_e32 v76, v76
	v_exp_f32_e32 v77, v77
	s_nop 0
	v_pk_add_f32 v[76:77], v[76:77], 1.0 op_sel_hi:[1,0]
	s_nop 0
	v_rcp_f32_e32 v76, v76
	v_rcp_f32_e32 v77, v77
	s_nop 0
	v_pk_mul_f32 v[68:69], v[76:77], v[68:69]
	v_cvt_pk_fp8_f32 v76, v74, v75
	v_cvt_pk_fp8_f32 v76, v72, v73 op_sel:[0,0,1]
	v_cvt_pk_fp8_f32 v73, v70, v71
	v_add_u32_e32 v70, 0x80, v93
	ds_bpermute_b32 v72, v92, v76
	v_cvt_pk_fp8_f32 v73, v68, v69 op_sel:[0,0,1]
	v_add_u32_e32 v68, 48, v93
	v_mad_i64_i32 v[68:69], s[10:11], v68, s9, v[10:11]
	ds_bpermute_b32 v73, v92, v73
	v_lshl_add_u64 v[68:69], v[68:69], 0, v[0:1]
	s_waitcnt lgkmcnt(0)
	global_store_dwordx2 v[68:69], v[72:73], off
	v_pk_mul_f32 v[68:69], v[128:129], v[64:65]
	v_pk_mul_f32 v[64:65], v[130:131], v[64:65]
	s_nop 0
	v_pk_mul_f32 v[64:65], v[64:65], v[66:67]
	v_exp_f32_e32 v66, v68
	v_exp_f32_e32 v67, v69
	s_nop 0
	v_pk_add_f32 v[66:67], v[66:67], 1.0 op_sel_hi:[1,0]
	s_nop 0
	v_rcp_f32_e32 v66, v66
	v_rcp_f32_e32 v67, v67
	s_nop 0
	v_pk_mul_f32 v[64:65], v[66:67], v[64:65]
	v_pk_mul_f32 v[66:67], v[128:129], v[62:63]
	v_pk_mul_f32 v[62:63], v[130:131], v[62:63]
	s_nop 0
	v_pk_mul_f32 v[34:35], v[62:63], v[34:35]
	v_exp_f32_e32 v62, v66
	v_exp_f32_e32 v63, v67
	s_nop 0
	v_pk_add_f32 v[62:63], v[62:63], 1.0 op_sel_hi:[1,0]
	s_nop 0
	v_rcp_f32_e32 v62, v62
	v_rcp_f32_e32 v63, v63
	s_nop 0
	v_pk_mul_f32 v[34:35], v[62:63], v[34:35]
	v_pk_mul_f32 v[62:63], v[128:129], v[60:61]
	v_pk_mul_f32 v[60:61], v[130:131], v[60:61]
	s_nop 0
	v_pk_mul_f32 v[30:31], v[60:61], v[30:31]
	v_exp_f32_e32 v60, v62
	v_exp_f32_e32 v61, v63
	s_nop 0
	v_pk_add_f32 v[60:61], v[60:61], 1.0 op_sel_hi:[1,0]
	s_nop 0
	v_rcp_f32_e32 v60, v60
	v_rcp_f32_e32 v61, v61
	s_nop 0
	v_pk_mul_f32 v[30:31], v[60:61], v[30:31]
	v_pk_mul_f32 v[60:61], v[128:129], v[58:59]
	v_pk_mul_f32 v[58:59], v[130:131], v[58:59]
	s_nop 0
	v_pk_mul_f32 v[28:29], v[58:59], v[28:29]
	v_exp_f32_e32 v58, v60
	v_exp_f32_e32 v59, v61
	s_nop 0
	v_pk_add_f32 v[58:59], v[58:59], 1.0 op_sel_hi:[1,0]
	s_nop 0
	v_rcp_f32_e32 v58, v58
	v_rcp_f32_e32 v59, v59
	s_nop 0
	v_pk_mul_f32 v[28:29], v[58:59], v[28:29]
	v_cvt_pk_fp8_f32 v58, v64, v65
	v_cvt_pk_fp8_f32 v58, v34, v35 op_sel:[0,0,1]
	v_cvt_pk_fp8_f32 v35, v30, v31
	v_pk_mul_f32 v[30:31], v[130:131], v[56:57]
	ds_bpermute_b32 v34, v92, v58
	v_pk_mul_f32 v[26:27], v[30:31], v[26:27]
	v_cvt_pk_fp8_f32 v35, v28, v29 op_sel:[0,0,1]
	v_mad_i64_i32 v[28:29], s[10:11], v70, s9, v[10:11]
	v_lshl_add_u64 v[28:29], v[28:29], 0, v[0:1]
	ds_bpermute_b32 v35, v92, v35
	v_pk_mul_f32 v[30:31], v[130:131], v[54:55]
	s_waitcnt lgkmcnt(0)
	global_store_dwordx2 v[28:29], v[34:35], off
	v_pk_mul_f32 v[28:29], v[128:129], v[56:57]
	v_pk_mul_f32 v[24:25], v[30:31], v[24:25]
	v_exp_f32_e32 v28, v28
	v_exp_f32_e32 v29, v29
	v_pk_mul_f32 v[30:31], v[130:131], v[52:53]
	v_pk_add_f32 v[28:29], v[28:29], 1.0 op_sel_hi:[1,0]
	s_nop 0
	v_rcp_f32_e32 v28, v28
	v_rcp_f32_e32 v29, v29
	v_pk_mul_f32 v[22:23], v[30:31], v[22:23]
	v_pk_mul_f32 v[30:31], v[130:131], v[50:51]
	v_pk_mul_f32 v[26:27], v[28:29], v[26:27]
	v_pk_mul_f32 v[28:29], v[128:129], v[54:55]
	v_pk_mul_f32 v[20:21], v[30:31], v[20:21]
	v_exp_f32_e32 v28, v28
	v_exp_f32_e32 v29, v29
	s_nop 0
	v_pk_add_f32 v[28:29], v[28:29], 1.0 op_sel_hi:[1,0]
	s_nop 0
	v_rcp_f32_e32 v28, v28
	v_rcp_f32_e32 v29, v29
	s_nop 0
	v_pk_mul_f32 v[24:25], v[28:29], v[24:25]
	v_pk_mul_f32 v[28:29], v[128:129], v[52:53]
	s_nop 0
	v_exp_f32_e32 v28, v28
	v_exp_f32_e32 v29, v29
	s_nop 0
	v_pk_add_f32 v[28:29], v[28:29], 1.0 op_sel_hi:[1,0]
	s_nop 0
	v_rcp_f32_e32 v28, v28
	v_rcp_f32_e32 v29, v29
	s_nop 0
	v_pk_mul_f32 v[22:23], v[28:29], v[22:23]
	v_pk_mul_f32 v[28:29], v[128:129], v[50:51]
	s_nop 0
	v_exp_f32_e32 v28, v28
	v_exp_f32_e32 v29, v29
	s_nop 0
	v_pk_add_f32 v[28:29], v[28:29], 1.0 op_sel_hi:[1,0]
	s_nop 0
	v_rcp_f32_e32 v28, v28
	v_rcp_f32_e32 v29, v29
	s_nop 0
	v_pk_mul_f32 v[20:21], v[28:29], v[20:21]
	v_cvt_pk_fp8_f32 v28, v26, v27
	v_cvt_pk_fp8_f32 v28, v24, v25 op_sel:[0,0,1]
	v_cvt_pk_fp8_f32 v25, v22, v23
	v_pk_mul_f32 v[22:23], v[130:131], v[48:49]
	ds_bpermute_b32 v24, v92, v28
	v_pk_mul_f32 v[18:19], v[22:23], v[18:19]
	v_cvt_pk_fp8_f32 v25, v20, v21 op_sel:[0,0,1]
	v_add_u32_e32 v20, 0x90, v93
	v_mad_i64_i32 v[20:21], s[10:11], v20, s9, v[10:11]
	ds_bpermute_b32 v25, v92, v25
	v_lshl_add_u64 v[20:21], v[20:21], 0, v[0:1]
	v_pk_mul_f32 v[22:23], v[130:131], v[46:47]
	s_waitcnt lgkmcnt(0)
	global_store_dwordx2 v[20:21], v[24:25], off
	v_pk_mul_f32 v[20:21], v[128:129], v[48:49]
	v_pk_mul_f32 v[16:17], v[22:23], v[16:17]
	v_exp_f32_e32 v20, v20
	v_exp_f32_e32 v21, v21
	v_pk_mul_f32 v[22:23], v[130:131], v[44:45]
	v_pk_add_f32 v[20:21], v[20:21], 1.0 op_sel_hi:[1,0]
	s_nop 0
	v_rcp_f32_e32 v20, v20
	v_rcp_f32_e32 v21, v21
	v_pk_mul_f32 v[14:15], v[22:23], v[14:15]
	v_pk_mul_f32 v[22:23], v[130:131], v[42:43]
	v_pk_mul_f32 v[18:19], v[20:21], v[18:19]
	v_pk_mul_f32 v[20:21], v[128:129], v[46:47]
	v_pk_mul_f32 v[12:13], v[22:23], v[12:13]
	v_exp_f32_e32 v20, v20
	v_exp_f32_e32 v21, v21
	s_nop 0
	v_pk_add_f32 v[20:21], v[20:21], 1.0 op_sel_hi:[1,0]
	s_nop 0
	v_rcp_f32_e32 v20, v20
	v_rcp_f32_e32 v21, v21
	s_nop 0
	v_pk_mul_f32 v[16:17], v[20:21], v[16:17]
	v_pk_mul_f32 v[20:21], v[128:129], v[44:45]
	s_nop 0
	v_exp_f32_e32 v20, v20
	v_exp_f32_e32 v21, v21
	s_nop 0
	v_pk_add_f32 v[20:21], v[20:21], 1.0 op_sel_hi:[1,0]
	s_nop 0
	v_rcp_f32_e32 v20, v20
	v_rcp_f32_e32 v21, v21
	s_nop 0
	v_pk_mul_f32 v[14:15], v[20:21], v[14:15]
	v_pk_mul_f32 v[20:21], v[128:129], v[42:43]
	s_nop 0
	v_exp_f32_e32 v20, v20
	v_exp_f32_e32 v21, v21
	s_nop 0
	v_pk_add_f32 v[20:21], v[20:21], 1.0 op_sel_hi:[1,0]
	s_nop 0
	v_rcp_f32_e32 v20, v20
	v_rcp_f32_e32 v21, v21
	s_nop 0
	v_pk_mul_f32 v[12:13], v[20:21], v[12:13]
	v_cvt_pk_fp8_f32 v20, v18, v19
	v_cvt_pk_fp8_f32 v20, v16, v17 op_sel:[0,0,1]
	v_cvt_pk_fp8_f32 v17, v14, v15
	v_pk_mul_f32 v[14:15], v[130:131], v[40:41]
	ds_bpermute_b32 v16, v92, v20
	v_pk_mul_f32 v[8:9], v[14:15], v[8:9]
	v_cvt_pk_fp8_f32 v17, v12, v13 op_sel:[0,0,1]
	v_add_u32_e32 v12, 0xa0, v93
	v_mad_i64_i32 v[12:13], s[10:11], v12, s9, v[10:11]
	ds_bpermute_b32 v17, v92, v17
	v_lshl_add_u64 v[12:13], v[12:13], 0, v[0:1]
	v_pk_mul_f32 v[14:15], v[130:131], v[38:39]
	s_waitcnt lgkmcnt(0)
	global_store_dwordx2 v[12:13], v[16:17], off
	v_pk_mul_f32 v[12:13], v[128:129], v[40:41]
	v_pk_mul_f32 v[6:7], v[14:15], v[6:7]
	v_exp_f32_e32 v12, v12
	v_exp_f32_e32 v13, v13
	v_pk_mul_f32 v[14:15], v[130:131], v[36:37]
	v_pk_add_f32 v[12:13], v[12:13], 1.0 op_sel_hi:[1,0]
	s_nop 0
	v_rcp_f32_e32 v12, v12
	v_rcp_f32_e32 v13, v13
	v_pk_mul_f32 v[4:5], v[14:15], v[4:5]
	v_pk_mul_f32 v[14:15], v[130:131], v[32:33]
	v_pk_mul_f32 v[8:9], v[12:13], v[8:9]
	v_pk_mul_f32 v[12:13], v[128:129], v[38:39]
	v_pk_mul_f32 v[2:3], v[14:15], v[2:3]
	v_exp_f32_e32 v12, v12
	v_exp_f32_e32 v13, v13
	s_nop 0
	v_pk_add_f32 v[12:13], v[12:13], 1.0 op_sel_hi:[1,0]
	s_nop 0
	v_rcp_f32_e32 v12, v12
	v_rcp_f32_e32 v13, v13
	s_nop 0
	v_pk_mul_f32 v[6:7], v[12:13], v[6:7]
	v_pk_mul_f32 v[12:13], v[128:129], v[36:37]
	s_nop 0
	v_exp_f32_e32 v12, v12
	v_exp_f32_e32 v13, v13
	s_nop 0
	v_pk_add_f32 v[12:13], v[12:13], 1.0 op_sel_hi:[1,0]
	s_nop 0
	v_rcp_f32_e32 v12, v12
	v_rcp_f32_e32 v13, v13
	s_nop 0
	v_pk_mul_f32 v[4:5], v[12:13], v[4:5]
	v_pk_mul_f32 v[12:13], v[128:129], v[32:33]
	s_nop 0
	v_exp_f32_e32 v12, v12
	v_exp_f32_e32 v13, v13
	s_nop 0
	v_pk_add_f32 v[12:13], v[12:13], 1.0 op_sel_hi:[1,0]
	s_nop 0
	v_rcp_f32_e32 v12, v12
	v_rcp_f32_e32 v13, v13
	s_nop 0
	v_pk_mul_f32 v[2:3], v[12:13], v[2:3]
	v_cvt_pk_fp8_f32 v12, v8, v9
	v_cvt_pk_fp8_f32 v12, v6, v7 op_sel:[0,0,1]
	v_cvt_pk_fp8_f32 v7, v4, v5
	ds_bpermute_b32 v6, v92, v12
	v_cvt_pk_fp8_f32 v7, v2, v3 op_sel:[0,0,1]
	v_add_u32_e32 v2, 0xb0, v93
	v_mad_i64_i32 v[2:3], s[10:11], v2, s9, v[10:11]
	ds_bpermute_b32 v7, v92, v7
	v_lshl_add_u64 v[0:1], v[2:3], 0, v[0:1]
	s_waitcnt lgkmcnt(0)
	global_store_dwordx2 v[0:1], v[6:7], off
	s_cbranch_vccnz .LBB0_1303
	s_andn2_b64 vcc, exec, s[20:21]
	s_cbranch_vccnz .LBB0_1302
	s_barrier
	s_branch .LBB0_1302

.LBB0_1469:
	s_cmp_gt_u32 s76, 13
	s_cselect_b64 s[54:55], -1, 0
	s_and_b64 vcc, s[54:55], exec
	s_cselect_b32 s54, -14, 2
	s_add_i32 s54, s54, s76
	s_ashr_i32 s55, s54, 31
	s_lshl_b64 s[54:55], s[54:55], 7
	s_add_u32 s56, s50, s54
	s_addc_u32 s57, s51, s55
	s_add_u32 s60, s48, s54
	s_addc_u32 s61, s49, s55
	s_cmp_gt_u32 s76, 12
	s_cselect_b32 s54, -13, 3
	s_add_i32 s54, s54, s76
	s_ashr_i32 s55, s54, 31
	s_lshl_b64 s[54:55], s[54:55], 7
	s_add_u32 s77, s50, s54
	s_addc_u32 s78, s51, s55
	s_add_u32 s79, s48, s54
	s_mov_b32 s54, s76
	v_add_u32_e32 v150, 0x10000, v136
	v_add_u32_e32 v166, 0x14000, v136
	ds_read_b128 v[138:141], v150
	ds_read_b128 v[142:145], v150 offset:1024
	ds_read_b128 v[146:149], v150 offset:2048
	ds_read_b128 v[150:153], v150 offset:3072
	ds_read_b128 v[154:157], v166
	ds_read_b128 v[158:161], v166 offset:1024
	ds_read_b128 v[162:165], v166 offset:2048
	ds_read_b128 v[166:169], v166 offset:3072
	s_addc_u32 s80, s49, s55
	s_cmp_eq_u32 s76, 14
	s_cselect_b32 s59, s23, s57
	s_cselect_b32 s58, s74, s56
	s_cselect_b32 s61, s41, s61
	s_cselect_b32 s60, s9, s60
	s_cselect_b32 s55, s11, s78
	s_cselect_b32 s54, s10, s77
	s_cselect_b32 s57, s75, s80
	s_cselect_b32 s56, s12, s79
	ds_read_b128 v[170:173], v137
	ds_read_b128 v[174:177], v137 offset:1024
	ds_read_b128 v[178:181], v137 offset:2048
	ds_read_b128 v[182:185], v137 offset:3072
	ds_read_b128 v[190:193], v137 offset:4096
	ds_read_b128 v[194:197], v137 offset:5120
	ds_read_b128 v[198:201], v137 offset:6144
	ds_read_b128 v[202:205], v137 offset:7168
	s_add_u32 s78, s52, 0x40080
	s_addc_u32 s79, s53, 0
	s_mov_b32 m0, s69
	s_nop 0
	global_load_lds_dwordx4 v132, s[78:79]
	s_add_i32 s77, s19, 0xe000
	s_mov_b32 m0, s77
	s_nop 0
	global_load_lds_dwordx4 v134, s[78:79]
	s_setprio 1
	s_waitcnt vmcnt(8)
	s_waitcnt lgkmcnt(0)
	s_barrier
	v_mfma_i32_16x16x64_i8 v[124:127], v[138:141], v[170:173], v[124:127]
	v_mfma_i32_16x16x64_i8 v[120:123], v[146:149], v[170:173], v[120:123]
	v_mfma_i32_16x16x64_i8 v[116:119], v[138:141], v[178:181], v[116:119]
	v_mfma_i32_16x16x64_i8 v[112:115], v[146:149], v[178:181], v[112:115]
	v_mfma_i32_16x16x64_i8 v[108:111], v[138:141], v[190:193], v[108:111]
	v_mfma_i32_16x16x64_i8 v[104:107], v[146:149], v[190:193], v[104:107]
	v_mfma_i32_16x16x64_i8 v[100:103], v[138:141], v[198:201], v[100:103]
	v_mfma_i32_16x16x64_i8 v[96:99], v[146:149], v[198:201], v[96:99]
	v_mfma_i32_16x16x64_i8 v[124:127], v[142:145], v[174:177], v[124:127]
	v_mfma_i32_16x16x64_i8 v[120:123], v[150:153], v[174:177], v[120:123]
	v_mfma_i32_16x16x64_i8 v[116:119], v[142:145], v[182:185], v[116:119]
	v_mfma_i32_16x16x64_i8 v[112:115], v[150:153], v[182:185], v[112:115]
	v_mfma_i32_16x16x64_i8 v[108:111], v[142:145], v[194:197], v[108:111]
	v_mfma_i32_16x16x64_i8 v[104:107], v[150:153], v[194:197], v[104:107]
	v_mfma_i32_16x16x64_i8 v[100:103], v[142:145], v[202:205], v[100:103]
	v_mfma_i32_16x16x64_i8 v[96:99], v[150:153], v[202:205], v[96:99]
	v_mfma_i32_16x16x64_i8 v[92:95], v[154:157], v[170:173], v[92:95]
	v_mfma_i32_16x16x64_i8 v[88:91], v[162:165], v[170:173], v[88:91]
	v_mfma_i32_16x16x64_i8 v[84:87], v[154:157], v[178:181], v[84:87]
	v_mfma_i32_16x16x64_i8 v[80:83], v[162:165], v[178:181], v[80:83]
	v_mfma_i32_16x16x64_i8 v[76:79], v[154:157], v[190:193], v[76:79]
	v_mfma_i32_16x16x64_i8 v[72:75], v[162:165], v[190:193], v[72:75]
	v_mfma_i32_16x16x64_i8 v[68:71], v[154:157], v[198:201], v[68:71]
	v_mfma_i32_16x16x64_i8 v[64:67], v[162:165], v[198:201], v[64:67]
	v_mfma_i32_16x16x64_i8 v[92:95], v[158:161], v[174:177], v[92:95]
	v_mfma_i32_16x16x64_i8 v[88:91], v[166:169], v[174:177], v[88:91]
	v_mfma_i32_16x16x64_i8 v[84:87], v[158:161], v[182:185], v[84:87]
	v_mfma_i32_16x16x64_i8 v[80:83], v[166:169], v[182:185], v[80:83]
	v_mfma_i32_16x16x64_i8 v[76:79], v[158:161], v[194:197], v[76:79]
	v_mfma_i32_16x16x64_i8 v[72:75], v[166:169], v[194:197], v[72:75]
	v_mfma_i32_16x16x64_i8 v[68:71], v[158:161], v[202:205], v[68:71]
	v_mfma_i32_16x16x64_i8 v[64:67], v[166:169], v[202:205], v[64:67]
	s_barrier
	s_setprio 0
	ds_read_b128 v[170:173], v137 offset:16384
	ds_read_b128 v[174:177], v137 offset:17408
	ds_read_b128 v[178:181], v137 offset:18432
	ds_read_b128 v[182:185], v137 offset:19456
	ds_read_b128 v[190:193], v137 offset:20480
	ds_read_b128 v[194:197], v137 offset:21504
	ds_read_b128 v[198:201], v137 offset:22528
	ds_read_b128 v[202:205], v137 offset:23552
	s_mov_b32 m0, s27
	s_nop 0
	global_load_lds_dwordx4 v133, s[60:61]
	s_nop 0
	s_mov_b32 m0, s28
	s_nop 0
	global_load_lds_dwordx4 v135, s[60:61]
	s_add_u32 s60, s60, 0x40000
	s_addc_u32 s61, s61, 0
	s_mov_b32 m0, s29
	s_nop 0
	global_load_lds_dwordx4 v133, s[60:61]
	s_nop 0
	s_mov_b32 m0, s30
	s_nop 0
	global_load_lds_dwordx4 v135, s[60:61]
	s_mov_b32 m0, s19
	s_nop 0
	global_load_lds_dwordx4 v132, s[58:59]
	s_nop 0
	s_mov_b32 m0, s31
	s_nop 0
	global_load_lds_dwordx4 v134, s[58:59]
	s_setprio 1
	s_waitcnt vmcnt(8)
	s_waitcnt lgkmcnt(0)
	s_barrier
	v_mfma_i32_16x16x64_i8 v[60:63], v[138:141], v[170:173], v[60:63]
	v_mfma_i32_16x16x64_i8 v[56:59], v[146:149], v[170:173], v[56:59]
	v_mfma_i32_16x16x64_i8 v[52:55], v[138:141], v[178:181], v[52:55]
	v_mfma_i32_16x16x64_i8 v[48:51], v[146:149], v[178:181], v[48:51]
	v_mfma_i32_16x16x64_i8 v[44:47], v[138:141], v[190:193], v[44:47]
	v_mfma_i32_16x16x64_i8 v[40:43], v[146:149], v[190:193], v[40:43]
	v_mfma_i32_16x16x64_i8 v[36:39], v[138:141], v[198:201], v[36:39]
	v_mfma_i32_16x16x64_i8 v[32:35], v[146:149], v[198:201], v[32:35]
	v_mfma_i32_16x16x64_i8 v[60:63], v[142:145], v[174:177], v[60:63]
	v_mfma_i32_16x16x64_i8 v[56:59], v[150:153], v[174:177], v[56:59]
	v_mfma_i32_16x16x64_i8 v[52:55], v[142:145], v[182:185], v[52:55]
	v_mfma_i32_16x16x64_i8 v[48:51], v[150:153], v[182:185], v[48:51]
	v_mfma_i32_16x16x64_i8 v[44:47], v[142:145], v[194:197], v[44:47]
	v_mfma_i32_16x16x64_i8 v[40:43], v[150:153], v[194:197], v[40:43]
	v_mfma_i32_16x16x64_i8 v[36:39], v[142:145], v[202:205], v[36:39]
	v_mfma_i32_16x16x64_i8 v[32:35], v[150:153], v[202:205], v[32:35]
	v_mfma_i32_16x16x64_i8 v[28:31], v[154:157], v[170:173], v[28:31]
	v_mfma_i32_16x16x64_i8 v[24:27], v[162:165], v[170:173], v[24:27]
	v_mfma_i32_16x16x64_i8 v[20:23], v[154:157], v[178:181], v[20:23]
	v_mfma_i32_16x16x64_i8 v[16:19], v[162:165], v[178:181], v[16:19]
	v_mfma_i32_16x16x64_i8 v[12:15], v[154:157], v[190:193], v[12:15]
	v_mfma_i32_16x16x64_i8 v[8:11], v[162:165], v[190:193], v[8:11]
	v_mfma_i32_16x16x64_i8 v[4:7], v[154:157], v[198:201], v[4:7]
	v_mfma_i32_16x16x64_i8 v[0:3], v[162:165], v[198:201], v[0:3]
	v_mfma_i32_16x16x64_i8 v[28:31], v[158:161], v[174:177], v[28:31]
	v_mfma_i32_16x16x64_i8 v[24:27], v[166:169], v[174:177], v[24:27]
	v_mfma_i32_16x16x64_i8 v[20:23], v[158:161], v[182:185], v[20:23]
	v_mfma_i32_16x16x64_i8 v[16:19], v[166:169], v[182:185], v[16:19]
	v_mfma_i32_16x16x64_i8 v[12:15], v[158:161], v[194:197], v[12:15]
	v_mfma_i32_16x16x64_i8 v[8:11], v[166:169], v[194:197], v[8:11]
	v_mfma_i32_16x16x64_i8 v[4:7], v[158:161], v[202:205], v[4:7]
	v_mfma_i32_16x16x64_i8 v[0:3], v[166:169], v[202:205], v[0:3]
	s_barrier
	s_setprio 0
	v_add_u32_e32 v150, 0x18000, v136
	v_add_u32_e32 v166, 0x1c000, v136
	ds_read_b128 v[138:141], v150
	ds_read_b128 v[142:145], v150 offset:1024
	ds_read_b128 v[146:149], v150 offset:2048
	ds_read_b128 v[150:153], v150 offset:3072
	ds_read_b128 v[154:157], v166
	ds_read_b128 v[158:161], v166 offset:1024
	ds_read_b128 v[162:165], v166 offset:2048
	ds_read_b128 v[166:169], v166 offset:3072
	ds_read_b128 v[170:173], v137 offset:32768
	ds_read_b128 v[174:177], v137 offset:33792
	ds_read_b128 v[178:181], v137 offset:34816
	ds_read_b128 v[182:185], v137 offset:35840
	ds_read_b128 v[190:193], v137 offset:36864
	ds_read_b128 v[194:197], v137 offset:37888
	ds_read_b128 v[198:201], v137 offset:38912
	ds_read_b128 v[202:205], v137 offset:39936
	s_add_u32 s58, s58, 0x40000
	s_addc_u32 s59, s59, 0
	s_mov_b32 m0, s34
	s_nop 0
	global_load_lds_dwordx4 v132, s[58:59]
	s_nop 0
	s_mov_b32 m0, s35
	s_nop 0
	global_load_lds_dwordx4 v134, s[58:59]
	s_setprio 1
	s_waitcnt vmcnt(8)
	s_waitcnt lgkmcnt(0)
	s_barrier
	v_mfma_i32_16x16x64_i8 v[124:127], v[138:141], v[170:173], v[124:127]
	v_mfma_i32_16x16x64_i8 v[120:123], v[146:149], v[170:173], v[120:123]
	v_mfma_i32_16x16x64_i8 v[116:119], v[138:141], v[178:181], v[116:119]
	v_mfma_i32_16x16x64_i8 v[112:115], v[146:149], v[178:181], v[112:115]
	v_mfma_i32_16x16x64_i8 v[108:111], v[138:141], v[190:193], v[108:111]
	v_mfma_i32_16x16x64_i8 v[104:107], v[146:149], v[190:193], v[104:107]
	v_mfma_i32_16x16x64_i8 v[100:103], v[138:141], v[198:201], v[100:103]
	v_mfma_i32_16x16x64_i8 v[96:99], v[146:149], v[198:201], v[96:99]
	v_mfma_i32_16x16x64_i8 v[124:127], v[142:145], v[174:177], v[124:127]
	v_mfma_i32_16x16x64_i8 v[120:123], v[150:153], v[174:177], v[120:123]
	v_mfma_i32_16x16x64_i8 v[116:119], v[142:145], v[182:185], v[116:119]
	v_mfma_i32_16x16x64_i8 v[112:115], v[150:153], v[182:185], v[112:115]
	v_mfma_i32_16x16x64_i8 v[108:111], v[142:145], v[194:197], v[108:111]
	v_mfma_i32_16x16x64_i8 v[104:107], v[150:153], v[194:197], v[104:107]
	v_mfma_i32_16x16x64_i8 v[100:103], v[142:145], v[202:205], v[100:103]
	v_mfma_i32_16x16x64_i8 v[96:99], v[150:153], v[202:205], v[96:99]
	v_mfma_i32_16x16x64_i8 v[92:95], v[154:157], v[170:173], v[92:95]
	v_mfma_i32_16x16x64_i8 v[88:91], v[162:165], v[170:173], v[88:91]
	v_mfma_i32_16x16x64_i8 v[84:87], v[154:157], v[178:181], v[84:87]
	v_mfma_i32_16x16x64_i8 v[80:83], v[162:165], v[178:181], v[80:83]
	v_mfma_i32_16x16x64_i8 v[76:79], v[154:157], v[190:193], v[76:79]
	v_mfma_i32_16x16x64_i8 v[72:75], v[162:165], v[190:193], v[72:75]
	v_mfma_i32_16x16x64_i8 v[68:71], v[154:157], v[198:201], v[68:71]
	v_mfma_i32_16x16x64_i8 v[64:67], v[162:165], v[198:201], v[64:67]
	v_mfma_i32_16x16x64_i8 v[92:95], v[158:161], v[174:177], v[92:95]
	v_mfma_i32_16x16x64_i8 v[88:91], v[166:169], v[174:177], v[88:91]
	v_mfma_i32_16x16x64_i8 v[84:87], v[158:161], v[182:185], v[84:87]
	v_mfma_i32_16x16x64_i8 v[80:83], v[166:169], v[182:185], v[80:83]
	v_mfma_i32_16x16x64_i8 v[76:79], v[158:161], v[194:197], v[76:79]
	v_mfma_i32_16x16x64_i8 v[72:75], v[166:169], v[194:197], v[72:75]
	v_mfma_i32_16x16x64_i8 v[68:71], v[158:161], v[202:205], v[68:71]
	v_mfma_i32_16x16x64_i8 v[64:67], v[166:169], v[202:205], v[64:67]
	s_barrier
	s_setprio 0
	ds_read_b128 v[170:173], v137 offset:49152
	ds_read_b128 v[174:177], v137 offset:50176
	ds_read_b128 v[178:181], v137 offset:51200
	ds_read_b128 v[182:185], v137 offset:52224
	ds_read_b128 v[190:193], v137 offset:53248
	ds_read_b128 v[194:197], v137 offset:54272
	ds_read_b128 v[198:201], v137 offset:55296
	ds_read_b128 v[202:205], v137 offset:56320
	s_mov_b32 m0, s62
	s_nop 0
	global_load_lds_dwordx4 v133, s[56:57]
	s_nop 0
	s_mov_b32 m0, s63
	s_nop 0
	global_load_lds_dwordx4 v135, s[56:57]
	s_add_u32 s56, s56, 0x40000
	s_addc_u32 s57, s57, 0
	s_mov_b32 m0, s67
	s_nop 0
	global_load_lds_dwordx4 v133, s[56:57]
	s_nop 0
	s_mov_b32 m0, s68
	s_nop 0
	global_load_lds_dwordx4 v135, s[56:57]
	s_mov_b32 m0, s65
	s_nop 0
	global_load_lds_dwordx4 v132, s[54:55]
	s_nop 0
	s_mov_b32 m0, s66
	s_nop 0
	global_load_lds_dwordx4 v134, s[54:55]
	s_setprio 1
	s_waitcnt vmcnt(8)
	s_waitcnt lgkmcnt(0)
	s_barrier
	v_mfma_i32_16x16x64_i8 v[60:63], v[138:141], v[170:173], v[60:63]
	v_mfma_i32_16x16x64_i8 v[56:59], v[146:149], v[170:173], v[56:59]
	v_mfma_i32_16x16x64_i8 v[52:55], v[138:141], v[178:181], v[52:55]
	v_mfma_i32_16x16x64_i8 v[48:51], v[146:149], v[178:181], v[48:51]
	v_mfma_i32_16x16x64_i8 v[44:47], v[138:141], v[190:193], v[44:47]
	v_mfma_i32_16x16x64_i8 v[40:43], v[146:149], v[190:193], v[40:43]
	v_mfma_i32_16x16x64_i8 v[36:39], v[138:141], v[198:201], v[36:39]
	v_mfma_i32_16x16x64_i8 v[32:35], v[146:149], v[198:201], v[32:35]
	v_mfma_i32_16x16x64_i8 v[60:63], v[142:145], v[174:177], v[60:63]
	v_mfma_i32_16x16x64_i8 v[56:59], v[150:153], v[174:177], v[56:59]
	v_mfma_i32_16x16x64_i8 v[52:55], v[142:145], v[182:185], v[52:55]
	v_mfma_i32_16x16x64_i8 v[48:51], v[150:153], v[182:185], v[48:51]
	v_mfma_i32_16x16x64_i8 v[44:47], v[142:145], v[194:197], v[44:47]
	v_mfma_i32_16x16x64_i8 v[40:43], v[150:153], v[194:197], v[40:43]
	v_mfma_i32_16x16x64_i8 v[36:39], v[142:145], v[202:205], v[36:39]
	v_mfma_i32_16x16x64_i8 v[32:35], v[150:153], v[202:205], v[32:35]
	v_mfma_i32_16x16x64_i8 v[28:31], v[154:157], v[170:173], v[28:31]
	v_mfma_i32_16x16x64_i8 v[24:27], v[162:165], v[170:173], v[24:27]
	v_mfma_i32_16x16x64_i8 v[20:23], v[154:157], v[178:181], v[20:23]
	v_mfma_i32_16x16x64_i8 v[16:19], v[162:165], v[178:181], v[16:19]
	v_mfma_i32_16x16x64_i8 v[12:15], v[154:157], v[190:193], v[12:15]
	v_mfma_i32_16x16x64_i8 v[8:11], v[162:165], v[190:193], v[8:11]
	v_mfma_i32_16x16x64_i8 v[4:7], v[154:157], v[198:201], v[4:7]
	v_mfma_i32_16x16x64_i8 v[0:3], v[162:165], v[198:201], v[0:3]
	v_mfma_i32_16x16x64_i8 v[28:31], v[158:161], v[174:177], v[28:31]
	v_mfma_i32_16x16x64_i8 v[24:27], v[166:169], v[174:177], v[24:27]
	v_mfma_i32_16x16x64_i8 v[20:23], v[158:161], v[182:185], v[20:23]
	v_mfma_i32_16x16x64_i8 v[16:19], v[166:169], v[182:185], v[16:19]
	v_mfma_i32_16x16x64_i8 v[12:15], v[158:161], v[194:197], v[12:15]
	v_mfma_i32_16x16x64_i8 v[8:11], v[166:169], v[194:197], v[8:11]
	v_mfma_i32_16x16x64_i8 v[4:7], v[158:161], v[202:205], v[4:7]
	v_mfma_i32_16x16x64_i8 v[0:3], v[166:169], v[202:205], v[0:3]
	s_barrier
	s_setprio 0
	s_add_i32 s76, s76, 2
	s_add_u32 s52, s52, 0x100
	s_addc_u32 s53, s53, 0
	s_cbranch_vccz .LBB0_1469
	v_cvt_f32_i32_e32 v124, v124
	v_cvt_f32_i32_e32 v125, v125
	v_cvt_f32_i32_e32 v140, v88
	v_cvt_f32_i32_e32 v88, v86
	v_cvt_f32_i32_e32 v86, v80
	v_cvt_f32_i32_e32 v80, v78
	v_cvt_f32_i32_e32 v78, v72
	v_cvt_f32_i32_e32 v72, v70
	v_cvt_f32_i32_e32 v70, v64
	v_cvt_f32_i32_e32 v64, v60
	v_cvt_f32_i32_e32 v60, v56
	v_cvt_f32_i32_e32 v56, v52
	v_cvt_f32_i32_e32 v52, v48
	v_cvt_f32_i32_e32 v48, v44
	v_cvt_f32_i32_e32 v44, v40
	v_cvt_f32_i32_e32 v40, v36
	v_cvt_f32_i32_e32 v36, v32
	v_cvt_f32_i32_e32 v32, v34
	v_cvt_f32_i32_e32 v34, v30
	v_cvt_f32_i32_e32 v30, v24
	v_cvt_f32_i32_e32 v24, v22
	v_cvt_f32_i32_e32 v22, v16
	v_cvt_f32_i32_e32 v16, v14
	v_cvt_f32_i32_e32 v14, v8
	v_cvt_f32_i32_e32 v8, v4
	v_cvt_f32_i32_e32 v4, v0
	v_mbcnt_lo_u32_b32 v0, -1, 0
	v_mbcnt_hi_u32_b32 v0, -1, v0
	s_lshl_b32 s9, s72, 8
	v_cvt_f32_i32_e32 v141, v89
	v_cvt_f32_i32_e32 v89, v87
	v_cvt_f32_i32_e32 v87, v81
	v_cvt_f32_i32_e32 v81, v79
	v_cvt_f32_i32_e32 v79, v73
	v_cvt_f32_i32_e32 v73, v71
	v_cvt_f32_i32_e32 v71, v65
	v_cvt_f32_i32_e32 v65, v61
	v_cvt_f32_i32_e32 v61, v57
	v_cvt_f32_i32_e32 v57, v53
	v_cvt_f32_i32_e32 v53, v49
	v_cvt_f32_i32_e32 v49, v45
	v_cvt_f32_i32_e32 v45, v41
	v_cvt_f32_i32_e32 v41, v37
	v_cvt_f32_i32_e32 v37, v33
	v_cvt_f32_i32_e32 v33, v35
	v_cvt_f32_i32_e32 v35, v31
	v_cvt_f32_i32_e32 v31, v25
	v_cvt_f32_i32_e32 v25, v23
	v_cvt_f32_i32_e32 v23, v17
	v_cvt_f32_i32_e32 v17, v15
	v_cvt_f32_i32_e32 v15, v9
	v_cvt_f32_i32_e32 v9, v5
	v_cvt_f32_i32_e32 v5, v1
	s_add_i32 s9, s9, s36
	v_ashrrev_i32_e32 v1, 2, v0
	v_cvt_f32_i32_e32 v139, v121
	v_cvt_f32_i32_e32 v121, v117
	v_cvt_f32_i32_e32 v117, v113
	v_cvt_f32_i32_e32 v113, v109
	v_cvt_f32_i32_e32 v109, v105
	v_cvt_f32_i32_e32 v105, v101
	v_cvt_f32_i32_e32 v101, v97
	v_cvt_f32_i32_e32 v97, v99
	v_cvt_f32_i32_e32 v99, v93
	v_cvt_f32_i32_e32 v142, v90
	v_cvt_f32_i32_e32 v90, v84
	v_cvt_f32_i32_e32 v84, v82
	v_cvt_f32_i32_e32 v82, v76
	v_cvt_f32_i32_e32 v76, v74
	v_cvt_f32_i32_e32 v74, v68
	v_cvt_f32_i32_e32 v68, v66
	v_cvt_f32_i32_e32 v66, v28
	v_cvt_f32_i32_e32 v28, v26
	v_cvt_f32_i32_e32 v26, v20
	v_cvt_f32_i32_e32 v20, v18
	v_cvt_f32_i32_e32 v18, v12
	v_cvt_f32_i32_e32 v12, v10
	v_and_b32_e32 v10, 3, v0
	v_and_b32_e32 v0, -4, v0
	v_add_u32_e32 v93, s9, v1
	s_lshl_b32 s9, s71, 7
	v_cvt_f32_i32_e32 v138, v120
	v_cvt_f32_i32_e32 v120, v116
	v_cvt_f32_i32_e32 v116, v112
	v_cvt_f32_i32_e32 v112, v108
	v_cvt_f32_i32_e32 v108, v104
	v_cvt_f32_i32_e32 v104, v100
	v_cvt_f32_i32_e32 v100, v96
	v_cvt_f32_i32_e32 v96, v98
	v_cvt_f32_i32_e32 v98, v92
	v_cvt_f32_i32_e32 v143, v91
	v_cvt_f32_i32_e32 v91, v85
	v_cvt_f32_i32_e32 v85, v83
	v_cvt_f32_i32_e32 v83, v77
	v_cvt_f32_i32_e32 v77, v75
	v_cvt_f32_i32_e32 v75, v69
	v_cvt_f32_i32_e32 v69, v67
	v_cvt_f32_i32_e32 v67, v29
	v_cvt_f32_i32_e32 v29, v27
	v_cvt_f32_i32_e32 v27, v21
	v_cvt_f32_i32_e32 v21, v19
	v_cvt_f32_i32_e32 v19, v13
	v_cvt_f32_i32_e32 v13, v11
	v_lshl_add_u32 v92, v10, 6, v0
	v_lshl_or_b32 v0, v10, 3, s9
	s_and_b64 vcc, exec, s[20:21]
	s_cbranch_vccz .LBB0_1472
	s_barrier
.LBB0_1472:
	v_pk_mul_f32 v[10:11], v[128:129], v[124:125]
	v_cvt_f32_i32_e32 v126, v126
	v_exp_f32_e32 v10, v10
	v_exp_f32_e32 v11, v11
	v_cvt_f32_i32_e32 v127, v127
	v_pk_mul_f32 v[124:125], v[130:131], v[124:125]
	v_cvt_f32_i32_e32 v94, v94
	v_pk_add_f32 v[10:11], v[10:11], 1.0 op_sel_hi:[1,0]
	v_pk_mul_f32 v[98:99], v[124:125], v[98:99]
	v_rcp_f32_e32 v10, v10
	v_rcp_f32_e32 v11, v11
	v_cvt_f32_i32_e32 v95, v95
	v_pk_mul_f32 v[124:125], v[130:131], v[126:127]
	v_cvt_f32_i32_e32 v122, v122
	v_pk_mul_f32 v[10:11], v[10:11], v[98:99]
	v_pk_mul_f32 v[98:99], v[128:129], v[126:127]
	v_pk_mul_f32 v[94:95], v[124:125], v[94:95]
	v_exp_f32_e32 v98, v98
	v_exp_f32_e32 v99, v99
	v_cvt_f32_i32_e32 v123, v123
	v_pk_mul_f32 v[124:125], v[130:131], v[138:139]
	v_or_b32_e32 v0, s37, v0
	v_pk_add_f32 v[98:99], v[98:99], 1.0 op_sel_hi:[1,0]
	v_pk_mul_f32 v[124:125], v[124:125], v[140:141]
	v_rcp_f32_e32 v98, v98
	v_rcp_f32_e32 v99, v99
	s_movk_i32 s9, 0x1600
	v_ashrrev_i32_e32 v1, 31, v0
	v_cvt_f32_i32_e32 v118, v118
	v_pk_mul_f32 v[94:95], v[98:99], v[94:95]
	v_pk_mul_f32 v[98:99], v[128:129], v[138:139]
	v_cvt_f32_i32_e32 v119, v119
	v_exp_f32_e32 v98, v98
	v_exp_f32_e32 v99, v99
	v_cvt_f32_i32_e32 v114, v114
	v_cvt_f32_i32_e32 v115, v115
	v_cvt_f32_i32_e32 v110, v110
	v_pk_add_f32 v[98:99], v[98:99], 1.0 op_sel_hi:[1,0]
	v_cvt_f32_i32_e32 v111, v111
	v_rcp_f32_e32 v98, v98
	v_rcp_f32_e32 v99, v99
	v_cvt_f32_i32_e32 v106, v106
	v_cvt_f32_i32_e32 v107, v107
	v_cvt_f32_i32_e32 v102, v102
	v_pk_mul_f32 v[98:99], v[98:99], v[124:125]
	v_pk_mul_f32 v[124:125], v[128:129], v[122:123]
	v_pk_mul_f32 v[122:123], v[130:131], v[122:123]
	v_exp_f32_e32 v124, v124
	v_exp_f32_e32 v125, v125
	v_pk_mul_f32 v[122:123], v[122:123], v[142:143]
	v_cvt_f32_i32_e32 v103, v103
	v_cvt_f32_i32_e32 v62, v62
	v_pk_add_f32 v[124:125], v[124:125], 1.0 op_sel_hi:[1,0]
	v_cvt_f32_i32_e32 v63, v63
	v_rcp_f32_e32 v124, v124
	v_rcp_f32_e32 v125, v125
	v_cvt_f32_i32_e32 v58, v58
	v_cvt_f32_i32_e32 v59, v59
	v_cvt_f32_i32_e32 v54, v54
	v_pk_mul_f32 v[122:123], v[124:125], v[122:123]
	v_cvt_pk_fp8_f32 v124, v10, v11
	v_cvt_pk_fp8_f32 v10, v98, v99
	v_cvt_f32_i32_e32 v55, v55
	v_cvt_pk_fp8_f32 v124, v94, v95 op_sel:[0,0,1]
	v_cvt_f32_i32_e32 v50, v50
	v_cvt_pk_fp8_f32 v10, v122, v123 op_sel:[0,0,1]
	v_cvt_f32_i32_e32 v51, v51
	ds_bpermute_b32 v94, v92, v124
	v_cvt_f32_i32_e32 v46, v46
	ds_bpermute_b32 v95, v92, v10
	v_mov_b64_e32 v[10:11], s[16:17]
	v_mad_i64_i32 v[98:99], s[10:11], v93, s9, v[10:11]
	v_lshl_add_u64 v[98:99], v[98:99], 0, v[0:1]
	s_waitcnt lgkmcnt(0)
	global_store_dwordx2 v[98:99], v[94:95], off
	v_pk_mul_f32 v[94:95], v[128:129], v[120:121]
	v_pk_mul_f32 v[98:99], v[130:131], v[120:121]
	v_exp_f32_e32 v94, v94
	v_exp_f32_e32 v95, v95
	v_pk_mul_f32 v[90:91], v[98:99], v[90:91]
	v_pk_mul_f32 v[98:99], v[130:131], v[118:119]
	v_cvt_f32_i32_e32 v47, v47
	v_pk_add_f32 v[94:95], v[94:95], 1.0 op_sel_hi:[1,0]
	v_pk_mul_f32 v[88:89], v[98:99], v[88:89]
	v_rcp_f32_e32 v94, v94
	v_rcp_f32_e32 v95, v95
	v_pk_mul_f32 v[98:99], v[130:131], v[116:117]
	v_cvt_f32_i32_e32 v42, v42
	v_pk_mul_f32 v[86:87], v[98:99], v[86:87]
	v_pk_mul_f32 v[90:91], v[94:95], v[90:91]
	v_pk_mul_f32 v[94:95], v[128:129], v[118:119]
	v_pk_mul_f32 v[98:99], v[130:131], v[114:115]
	v_exp_f32_e32 v94, v94
	v_exp_f32_e32 v95, v95
	v_pk_mul_f32 v[84:85], v[98:99], v[84:85]
	v_cvt_f32_i32_e32 v43, v43
	v_cvt_f32_i32_e32 v38, v38
	v_pk_add_f32 v[94:95], v[94:95], 1.0 op_sel_hi:[1,0]
	v_cvt_f32_i32_e32 v39, v39
	v_rcp_f32_e32 v94, v94
	v_rcp_f32_e32 v95, v95
	v_cvt_f32_i32_e32 v6, v6
	v_cvt_f32_i32_e32 v7, v7
	v_cvt_f32_i32_e32 v2, v2
	v_pk_mul_f32 v[88:89], v[94:95], v[88:89]
	v_pk_mul_f32 v[94:95], v[128:129], v[116:117]
	v_cvt_f32_i32_e32 v3, v3
	v_exp_f32_e32 v94, v94
	v_exp_f32_e32 v95, v95
	s_mov_b64 s[48:49], -1
	s_andn2_b64 vcc, exec, s[42:43]
	v_pk_add_f32 v[94:95], v[94:95], 1.0 op_sel_hi:[1,0]
	s_nop 0
	v_rcp_f32_e32 v94, v94
	v_rcp_f32_e32 v95, v95
	s_nop 0
	v_pk_mul_f32 v[86:87], v[94:95], v[86:87]
	v_pk_mul_f32 v[94:95], v[128:129], v[114:115]
	s_nop 0
	v_exp_f32_e32 v94, v94
	v_exp_f32_e32 v95, v95
	s_nop 0
	v_pk_add_f32 v[94:95], v[94:95], 1.0 op_sel_hi:[1,0]
	s_nop 0
	v_rcp_f32_e32 v94, v94
	v_rcp_f32_e32 v95, v95
	s_nop 0
	v_pk_mul_f32 v[84:85], v[94:95], v[84:85]
	v_cvt_pk_fp8_f32 v94, v90, v91
	v_cvt_pk_fp8_f32 v94, v88, v89 op_sel:[0,0,1]
	v_cvt_pk_fp8_f32 v89, v86, v87
	v_pk_mul_f32 v[86:87], v[130:131], v[112:113]
	ds_bpermute_b32 v88, v92, v94
	v_pk_mul_f32 v[82:83], v[86:87], v[82:83]
	v_cvt_pk_fp8_f32 v89, v84, v85 op_sel:[0,0,1]
	v_add_u32_e32 v84, 16, v93
	v_mad_i64_i32 v[84:85], s[10:11], v84, s9, v[10:11]
	ds_bpermute_b32 v89, v92, v89
	v_lshl_add_u64 v[84:85], v[84:85], 0, v[0:1]
	v_pk_mul_f32 v[86:87], v[130:131], v[110:111]
	s_waitcnt lgkmcnt(0)
	global_store_dwordx2 v[84:85], v[88:89], off
	v_pk_mul_f32 v[84:85], v[128:129], v[112:113]
	v_pk_mul_f32 v[80:81], v[86:87], v[80:81]
	v_exp_f32_e32 v84, v84
	v_exp_f32_e32 v85, v85
	v_pk_mul_f32 v[86:87], v[130:131], v[108:109]
	v_pk_add_f32 v[84:85], v[84:85], 1.0 op_sel_hi:[1,0]
	s_nop 0
	v_rcp_f32_e32 v84, v84
	v_rcp_f32_e32 v85, v85
	v_pk_mul_f32 v[78:79], v[86:87], v[78:79]
	v_pk_mul_f32 v[86:87], v[130:131], v[106:107]
	v_pk_mul_f32 v[82:83], v[84:85], v[82:83]
	v_pk_mul_f32 v[84:85], v[128:129], v[110:111]
	v_pk_mul_f32 v[76:77], v[86:87], v[76:77]
	v_exp_f32_e32 v84, v84
	v_exp_f32_e32 v85, v85
	s_nop 0
	v_pk_add_f32 v[84:85], v[84:85], 1.0 op_sel_hi:[1,0]
	s_nop 0
	v_rcp_f32_e32 v84, v84
	v_rcp_f32_e32 v85, v85
	s_nop 0
	v_pk_mul_f32 v[80:81], v[84:85], v[80:81]
	v_pk_mul_f32 v[84:85], v[128:129], v[108:109]
	s_nop 0
	v_exp_f32_e32 v84, v84
	v_exp_f32_e32 v85, v85
	s_nop 0
	v_pk_add_f32 v[84:85], v[84:85], 1.0 op_sel_hi:[1,0]
	s_nop 0
	v_rcp_f32_e32 v84, v84
	v_rcp_f32_e32 v85, v85
	s_nop 0
	v_pk_mul_f32 v[78:79], v[84:85], v[78:79]
	v_pk_mul_f32 v[84:85], v[128:129], v[106:107]
	s_nop 0
	v_exp_f32_e32 v84, v84
	v_exp_f32_e32 v85, v85
	s_nop 0
	v_pk_add_f32 v[84:85], v[84:85], 1.0 op_sel_hi:[1,0]
	s_nop 0
	v_rcp_f32_e32 v84, v84
	v_rcp_f32_e32 v85, v85
	s_nop 0
	v_pk_mul_f32 v[76:77], v[84:85], v[76:77]
	v_cvt_pk_fp8_f32 v84, v82, v83
	v_cvt_pk_fp8_f32 v84, v80, v81 op_sel:[0,0,1]
	v_cvt_pk_fp8_f32 v81, v78, v79
	v_pk_mul_f32 v[78:79], v[130:131], v[104:105]
	ds_bpermute_b32 v80, v92, v84
	v_pk_mul_f32 v[74:75], v[78:79], v[74:75]
	v_cvt_pk_fp8_f32 v81, v76, v77 op_sel:[0,0,1]
	v_add_u32_e32 v76, 32, v93
	v_mad_i64_i32 v[76:77], s[10:11], v76, s9, v[10:11]
	ds_bpermute_b32 v81, v92, v81
	v_lshl_add_u64 v[76:77], v[76:77], 0, v[0:1]
	v_pk_mul_f32 v[78:79], v[130:131], v[102:103]
	s_waitcnt lgkmcnt(0)
	global_store_dwordx2 v[76:77], v[80:81], off
	v_pk_mul_f32 v[76:77], v[128:129], v[104:105]
	v_pk_mul_f32 v[72:73], v[78:79], v[72:73]
	v_exp_f32_e32 v76, v76
	v_exp_f32_e32 v77, v77
	v_pk_mul_f32 v[78:79], v[130:131], v[100:101]
	v_pk_add_f32 v[76:77], v[76:77], 1.0 op_sel_hi:[1,0]
	s_nop 0
	v_rcp_f32_e32 v76, v76
	v_rcp_f32_e32 v77, v77
	v_pk_mul_f32 v[70:71], v[78:79], v[70:71]
	v_pk_mul_f32 v[78:79], v[130:131], v[96:97]
	v_pk_mul_f32 v[74:75], v[76:77], v[74:75]
	v_pk_mul_f32 v[76:77], v[128:129], v[102:103]
	v_pk_mul_f32 v[68:69], v[78:79], v[68:69]
	v_exp_f32_e32 v76, v76
	v_exp_f32_e32 v77, v77
	s_nop 0
	v_pk_add_f32 v[76:77], v[76:77], 1.0 op_sel_hi:[1,0]
	s_nop 0
	v_rcp_f32_e32 v76, v76
	v_rcp_f32_e32 v77, v77
	s_nop 0
	v_pk_mul_f32 v[72:73], v[76:77], v[72:73]
	v_pk_mul_f32 v[76:77], v[128:129], v[100:101]
	s_nop 0
	v_exp_f32_e32 v76, v76
	v_exp_f32_e32 v77, v77
	s_nop 0
	v_pk_add_f32 v[76:77], v[76:77], 1.0 op_sel_hi:[1,0]
	s_nop 0
	v_rcp_f32_e32 v76, v76
	v_rcp_f32_e32 v77, v77
	s_nop 0
	v_pk_mul_f32 v[70:71], v[76:77], v[70:71]
	v_pk_mul_f32 v[76:77], v[128:129], v[96:97]
	s_nop 0
	v_exp_f32_e32 v76, v76
	v_exp_f32_e32 v77, v77
	s_nop 0
	v_pk_add_f32 v[76:77], v[76:77], 1.0 op_sel_hi:[1,0]
	s_nop 0
	v_rcp_f32_e32 v76, v76
	v_rcp_f32_e32 v77, v77
	s_nop 0
	v_pk_mul_f32 v[68:69], v[76:77], v[68:69]
	v_cvt_pk_fp8_f32 v76, v74, v75
	v_cvt_pk_fp8_f32 v76, v72, v73 op_sel:[0,0,1]
	v_cvt_pk_fp8_f32 v73, v70, v71
	v_add_u32_e32 v70, 0x80, v93
	ds_bpermute_b32 v72, v92, v76
	v_cvt_pk_fp8_f32 v73, v68, v69 op_sel:[0,0,1]
	v_add_u32_e32 v68, 48, v93
	v_mad_i64_i32 v[68:69], s[10:11], v68, s9, v[10:11]
	ds_bpermute_b32 v73, v92, v73
	v_lshl_add_u64 v[68:69], v[68:69], 0, v[0:1]
	s_waitcnt lgkmcnt(0)
	global_store_dwordx2 v[68:69], v[72:73], off
	v_pk_mul_f32 v[68:69], v[128:129], v[64:65]
	v_pk_mul_f32 v[64:65], v[130:131], v[64:65]
	s_nop 0
	v_pk_mul_f32 v[64:65], v[64:65], v[66:67]
	v_exp_f32_e32 v66, v68
	v_exp_f32_e32 v67, v69
	s_nop 0
	v_pk_add_f32 v[66:67], v[66:67], 1.0 op_sel_hi:[1,0]
	s_nop 0
	v_rcp_f32_e32 v66, v66
	v_rcp_f32_e32 v67, v67
	s_nop 0
	v_pk_mul_f32 v[64:65], v[66:67], v[64:65]
	v_pk_mul_f32 v[66:67], v[128:129], v[62:63]
	v_pk_mul_f32 v[62:63], v[130:131], v[62:63]
	s_nop 0
	v_pk_mul_f32 v[34:35], v[62:63], v[34:35]
	v_exp_f32_e32 v62, v66
	v_exp_f32_e32 v63, v67
	s_nop 0
	v_pk_add_f32 v[62:63], v[62:63], 1.0 op_sel_hi:[1,0]
	s_nop 0
	v_rcp_f32_e32 v62, v62
	v_rcp_f32_e32 v63, v63
	s_nop 0
	v_pk_mul_f32 v[34:35], v[62:63], v[34:35]
	v_pk_mul_f32 v[62:63], v[128:129], v[60:61]
	v_pk_mul_f32 v[60:61], v[130:131], v[60:61]
	s_nop 0
	v_pk_mul_f32 v[30:31], v[60:61], v[30:31]
	v_exp_f32_e32 v60, v62
	v_exp_f32_e32 v61, v63
	s_nop 0
	v_pk_add_f32 v[60:61], v[60:61], 1.0 op_sel_hi:[1,0]
	s_nop 0
	v_rcp_f32_e32 v60, v60
	v_rcp_f32_e32 v61, v61
	s_nop 0
	v_pk_mul_f32 v[30:31], v[60:61], v[30:31]
	v_pk_mul_f32 v[60:61], v[128:129], v[58:59]
	v_pk_mul_f32 v[58:59], v[130:131], v[58:59]
	s_nop 0
	v_pk_mul_f32 v[28:29], v[58:59], v[28:29]
	v_exp_f32_e32 v58, v60
	v_exp_f32_e32 v59, v61
	s_nop 0
	v_pk_add_f32 v[58:59], v[58:59], 1.0 op_sel_hi:[1,0]
	s_nop 0
	v_rcp_f32_e32 v58, v58
	v_rcp_f32_e32 v59, v59
	s_nop 0
	v_pk_mul_f32 v[28:29], v[58:59], v[28:29]
	v_cvt_pk_fp8_f32 v58, v64, v65
	v_cvt_pk_fp8_f32 v58, v34, v35 op_sel:[0,0,1]
	v_cvt_pk_fp8_f32 v35, v30, v31
	v_pk_mul_f32 v[30:31], v[130:131], v[56:57]
	ds_bpermute_b32 v34, v92, v58
	v_pk_mul_f32 v[26:27], v[30:31], v[26:27]
	v_cvt_pk_fp8_f32 v35, v28, v29 op_sel:[0,0,1]
	v_mad_i64_i32 v[28:29], s[10:11], v70, s9, v[10:11]
	v_lshl_add_u64 v[28:29], v[28:29], 0, v[0:1]
	ds_bpermute_b32 v35, v92, v35
	v_pk_mul_f32 v[30:31], v[130:131], v[54:55]
	s_waitcnt lgkmcnt(0)
	global_store_dwordx2 v[28:29], v[34:35], off
	v_pk_mul_f32 v[28:29], v[128:129], v[56:57]
	v_pk_mul_f32 v[24:25], v[30:31], v[24:25]
	v_exp_f32_e32 v28, v28
	v_exp_f32_e32 v29, v29
	v_pk_mul_f32 v[30:31], v[130:131], v[52:53]
	v_pk_add_f32 v[28:29], v[28:29], 1.0 op_sel_hi:[1,0]
	s_nop 0
	v_rcp_f32_e32 v28, v28
	v_rcp_f32_e32 v29, v29
	v_pk_mul_f32 v[22:23], v[30:31], v[22:23]
	v_pk_mul_f32 v[30:31], v[130:131], v[50:51]
	v_pk_mul_f32 v[26:27], v[28:29], v[26:27]
	v_pk_mul_f32 v[28:29], v[128:129], v[54:55]
	v_pk_mul_f32 v[20:21], v[30:31], v[20:21]
	v_exp_f32_e32 v28, v28
	v_exp_f32_e32 v29, v29
	s_nop 0
	v_pk_add_f32 v[28:29], v[28:29], 1.0 op_sel_hi:[1,0]
	s_nop 0
	v_rcp_f32_e32 v28, v28
	v_rcp_f32_e32 v29, v29
	s_nop 0
	v_pk_mul_f32 v[24:25], v[28:29], v[24:25]
	v_pk_mul_f32 v[28:29], v[128:129], v[52:53]
	s_nop 0
	v_exp_f32_e32 v28, v28
	v_exp_f32_e32 v29, v29
	s_nop 0
	v_pk_add_f32 v[28:29], v[28:29], 1.0 op_sel_hi:[1,0]
	s_nop 0
	v_rcp_f32_e32 v28, v28
	v_rcp_f32_e32 v29, v29
	s_nop 0
	v_pk_mul_f32 v[22:23], v[28:29], v[22:23]
	v_pk_mul_f32 v[28:29], v[128:129], v[50:51]
	s_nop 0
	v_exp_f32_e32 v28, v28
	v_exp_f32_e32 v29, v29
	s_nop 0
	v_pk_add_f32 v[28:29], v[28:29], 1.0 op_sel_hi:[1,0]
	s_nop 0
	v_rcp_f32_e32 v28, v28
	v_rcp_f32_e32 v29, v29
	s_nop 0
	v_pk_mul_f32 v[20:21], v[28:29], v[20:21]
	v_cvt_pk_fp8_f32 v28, v26, v27
	v_cvt_pk_fp8_f32 v28, v24, v25 op_sel:[0,0,1]
	v_cvt_pk_fp8_f32 v25, v22, v23
	v_pk_mul_f32 v[22:23], v[130:131], v[48:49]
	ds_bpermute_b32 v24, v92, v28
	v_pk_mul_f32 v[18:19], v[22:23], v[18:19]
	v_cvt_pk_fp8_f32 v25, v20, v21 op_sel:[0,0,1]
	v_add_u32_e32 v20, 0x90, v93
	v_mad_i64_i32 v[20:21], s[10:11], v20, s9, v[10:11]
	ds_bpermute_b32 v25, v92, v25
	v_lshl_add_u64 v[20:21], v[20:21], 0, v[0:1]
	v_pk_mul_f32 v[22:23], v[130:131], v[46:47]
	s_waitcnt lgkmcnt(0)
	global_store_dwordx2 v[20:21], v[24:25], off
	v_pk_mul_f32 v[20:21], v[128:129], v[48:49]
	v_pk_mul_f32 v[16:17], v[22:23], v[16:17]
	v_exp_f32_e32 v20, v20
	v_exp_f32_e32 v21, v21
	v_pk_mul_f32 v[22:23], v[130:131], v[44:45]
	v_pk_add_f32 v[20:21], v[20:21], 1.0 op_sel_hi:[1,0]
	s_nop 0
	v_rcp_f32_e32 v20, v20
	v_rcp_f32_e32 v21, v21
	v_pk_mul_f32 v[14:15], v[22:23], v[14:15]
	v_pk_mul_f32 v[22:23], v[130:131], v[42:43]
	v_pk_mul_f32 v[18:19], v[20:21], v[18:19]
	v_pk_mul_f32 v[20:21], v[128:129], v[46:47]
	v_pk_mul_f32 v[12:13], v[22:23], v[12:13]
	v_exp_f32_e32 v20, v20
	v_exp_f32_e32 v21, v21
	s_nop 0
	v_pk_add_f32 v[20:21], v[20:21], 1.0 op_sel_hi:[1,0]
	s_nop 0
	v_rcp_f32_e32 v20, v20
	v_rcp_f32_e32 v21, v21
	s_nop 0
	v_pk_mul_f32 v[16:17], v[20:21], v[16:17]
	v_pk_mul_f32 v[20:21], v[128:129], v[44:45]
	s_nop 0
	v_exp_f32_e32 v20, v20
	v_exp_f32_e32 v21, v21
	s_nop 0
	v_pk_add_f32 v[20:21], v[20:21], 1.0 op_sel_hi:[1,0]
	s_nop 0
	v_rcp_f32_e32 v20, v20
	v_rcp_f32_e32 v21, v21
	s_nop 0
	v_pk_mul_f32 v[14:15], v[20:21], v[14:15]
	v_pk_mul_f32 v[20:21], v[128:129], v[42:43]
	s_nop 0
	v_exp_f32_e32 v20, v20
	v_exp_f32_e32 v21, v21
	s_nop 0
	v_pk_add_f32 v[20:21], v[20:21], 1.0 op_sel_hi:[1,0]
	s_nop 0
	v_rcp_f32_e32 v20, v20
	v_rcp_f32_e32 v21, v21
	s_nop 0
	v_pk_mul_f32 v[12:13], v[20:21], v[12:13]
	v_cvt_pk_fp8_f32 v20, v18, v19
	v_cvt_pk_fp8_f32 v20, v16, v17 op_sel:[0,0,1]
	v_cvt_pk_fp8_f32 v17, v14, v15
	v_pk_mul_f32 v[14:15], v[130:131], v[40:41]
	ds_bpermute_b32 v16, v92, v20
	v_pk_mul_f32 v[8:9], v[14:15], v[8:9]
	v_cvt_pk_fp8_f32 v17, v12, v13 op_sel:[0,0,1]
	v_add_u32_e32 v12, 0xa0, v93
	v_mad_i64_i32 v[12:13], s[10:11], v12, s9, v[10:11]
	ds_bpermute_b32 v17, v92, v17
	v_lshl_add_u64 v[12:13], v[12:13], 0, v[0:1]
	v_pk_mul_f32 v[14:15], v[130:131], v[38:39]
	s_waitcnt lgkmcnt(0)
	global_store_dwordx2 v[12:13], v[16:17], off
	v_pk_mul_f32 v[12:13], v[128:129], v[40:41]
	v_pk_mul_f32 v[6:7], v[14:15], v[6:7]
	v_exp_f32_e32 v12, v12
	v_exp_f32_e32 v13, v13
	v_pk_mul_f32 v[14:15], v[130:131], v[36:37]
	v_pk_add_f32 v[12:13], v[12:13], 1.0 op_sel_hi:[1,0]
	s_nop 0
	v_rcp_f32_e32 v12, v12
	v_rcp_f32_e32 v13, v13
	v_pk_mul_f32 v[4:5], v[14:15], v[4:5]
	v_pk_mul_f32 v[14:15], v[130:131], v[32:33]
	v_pk_mul_f32 v[8:9], v[12:13], v[8:9]
	v_pk_mul_f32 v[12:13], v[128:129], v[38:39]
	v_pk_mul_f32 v[2:3], v[14:15], v[2:3]
	v_exp_f32_e32 v12, v12
	v_exp_f32_e32 v13, v13
	s_nop 0
	v_pk_add_f32 v[12:13], v[12:13], 1.0 op_sel_hi:[1,0]
	s_nop 0
	v_rcp_f32_e32 v12, v12
	v_rcp_f32_e32 v13, v13
	s_nop 0
	v_pk_mul_f32 v[6:7], v[12:13], v[6:7]
	v_pk_mul_f32 v[12:13], v[128:129], v[36:37]
	s_nop 0
	v_exp_f32_e32 v12, v12
	v_exp_f32_e32 v13, v13
	s_nop 0
	v_pk_add_f32 v[12:13], v[12:13], 1.0 op_sel_hi:[1,0]
	s_nop 0
	v_rcp_f32_e32 v12, v12
	v_rcp_f32_e32 v13, v13
	s_nop 0
	v_pk_mul_f32 v[4:5], v[12:13], v[4:5]
	v_pk_mul_f32 v[12:13], v[128:129], v[32:33]
	s_nop 0
	v_exp_f32_e32 v12, v12
	v_exp_f32_e32 v13, v13
	s_nop 0
	v_pk_add_f32 v[12:13], v[12:13], 1.0 op_sel_hi:[1,0]
	s_nop 0
	v_rcp_f32_e32 v12, v12
	v_rcp_f32_e32 v13, v13
	s_nop 0
	v_pk_mul_f32 v[2:3], v[12:13], v[2:3]
	v_cvt_pk_fp8_f32 v12, v8, v9
	v_cvt_pk_fp8_f32 v12, v6, v7 op_sel:[0,0,1]
	v_cvt_pk_fp8_f32 v7, v4, v5
	ds_bpermute_b32 v6, v92, v12
	v_cvt_pk_fp8_f32 v7, v2, v3 op_sel:[0,0,1]
	v_add_u32_e32 v2, 0xb0, v93
	v_mad_i64_i32 v[2:3], s[10:11], v2, s9, v[10:11]
	ds_bpermute_b32 v7, v92, v7
	v_lshl_add_u64 v[0:1], v[2:3], 0, v[0:1]
	s_waitcnt lgkmcnt(0)
	global_store_dwordx2 v[0:1], v[6:7], off
	s_cbranch_vccnz .LBB0_1465
	s_andn2_b64 vcc, exec, s[0:1]
	s_cbranch_vccnz .LBB0_1464
	s_barrier
	s_branch .LBB0_1464
